# v14 + nt on prologue weight-conversion stores and final output stores
# baseline (speedup 1.0000x reference)
; #define LAS __attribute__((address_space(3)))
; __device__ __forceinline__ unsigned cvt_pk_bf16(float lo, float hi) { unsigned r; asm volatile("v_cvt_pk_bf16_f32 %0, %1, %2" : "=v"(r) : "v"(lo), "v"(hi)); return r; }
; #define CVT_LOAD(jx) do { const int b_ = (jx) / per, r_ = (jx) - b_ * per, kt_ = r_ / tn, nt_ = r_ - kt_ * tn; \
;         const float* s_ = src + (size_t)b_ * sbs + (size_t)(kt_ * 64) * ldS + nt_ * 256; \
;         _Pragma("unroll") for (int q = 0; q < 8; ++q) v[q] = *(const float4*)(s_ + (size_t)(kr + 8 * q) * ldS + c4 * 4); } while (0)
;     ...
;         const int b = j / per, r = j - b * per, kt = r / tn, ntile = r - kt * tn;
;         __syncthreads();
; #pragma unroll
;         for (int q = 0; q < 8; ++q) { LAS float* tp = tile + (kr + 8 * q) * 257 + c4 * 4; tp[0] = v[q].x; tp[1] = v[q].y; tp[2] = v[q].z; tp[3] = v[q].w; }
;         if (j + G < total) CVT_LOAD(j + G);
;         __syncthreads();
;         bf16_t* dmat = dst + (size_t)b * dbs;
; #pragma unroll
;         for (int q = 0; q < 4; ++q) {
;             const int id = tid + NTHR * q, nr = id >> 3, kc = id & 7;
;             const int n = ntile * 256 + nr;
;             const int drow = (mode == 0) ? n : ((n >> 7) * 256 + (mode == 2 ? 128 : 0) + (n & 127));
;             const LAS float* tp = tile + (kc * 8) * 257 + nr;
;             u32x4 w; w.x = cvt_pk_bf16(tp[0], tp[257]); w.y = cvt_pk_bf16(tp[2 * 257], tp[3 * 257]); w.z = cvt_pk_bf16(tp[4 * 257], tp[5 * 257]); w.w = cvt_pk_bf16(tp[6 * 257], tp[7 * 257]);
;             if (nrimg) *(u32x4*)(dmat + ((size_t)(kt * 8 + kc) * nrimg + drow) * 8) = w;
;             else *(u32x4*)(dmat + (size_t)drow * K + kt * 64 + kc * 8) = w;
.LBB0_93:
	s_waitcnt lgkmcnt(0)
	s_barrier
	ds_read_b32 v62, v54 offset:1028
	ds_read_b32 v63, v54
	s_mul_hi_i32 s10, s9, 0x2aaaaaab
	s_waitcnt lgkmcnt(0)
	v_cvt_pk_bf16_f32 v62, v63, v62
	ds_read_b32 v63, v54 offset:3084
	ds_read_b32 v64, v54 offset:2056
	s_waitcnt lgkmcnt(0)
	v_cvt_pk_bf16_f32 v63, v64, v63
	ds_read_b32 v64, v54 offset:5140
	ds_read_b32 v65, v54 offset:4112
	s_lshr_b32 s11, s10, 31
	s_lshr_b32 s10, s10, 7
	s_add_i32 s10, s10, s11
	s_mulk_i32 s10, 0x300
	s_sub_i32 s9, s9, s10
	s_mul_i32 s10, s9, 0x2aab
	s_waitcnt lgkmcnt(0)
	v_cvt_pk_bf16_f32 v64, v65, v64
	ds_read_b32 v65, v54 offset:7196
	ds_read_b32 v69, v54 offset:6168
	s_lshr_b32 s11, s10, 31
	s_ashr_i32 s10, s10, 18
	s_add_i32 s10, s10, s11
	s_mul_i32 s11, s10, 0xffffffe8
	s_add_i32 s11, s11, s9
	s_lshl_b32 s9, s11, 8
	s_waitcnt lgkmcnt(0)
	v_cvt_pk_bf16_f32 v65, v69, v65
	ds_read_b32 v70, v56 offset:1028
	ds_read_b32 v71, v56
	s_lshl_b32 s10, s10, 6
	v_add_u32_e32 v68, s9, v1
	s_ashr_i32 s11, s10, 31
	v_ashrrev_i32_e32 v69, 31, v68
	v_lshl_add_u64 v[66:67], s[10:11], 1, v[52:53]
	v_lshlrev_b64 v[68:69], 12, v[68:69]
	v_lshl_add_u64 v[68:69], v[66:67], 0, v[68:69]
	global_store_dwordx4 v[68:69], v[62:65], off nt
	v_add_u32_e32 v68, s9, v55
	s_andn2_b64 vcc, exec, s[6:7]
	s_waitcnt lgkmcnt(0)
	v_cvt_pk_bf16_f32 v62, v71, v70
	ds_read_b32 v63, v56 offset:3084
	ds_read_b32 v64, v56 offset:2056
	s_waitcnt lgkmcnt(0)
	v_cvt_pk_bf16_f32 v63, v64, v63
	ds_read_b32 v64, v56 offset:5140
	ds_read_b32 v65, v56 offset:4112
	s_waitcnt lgkmcnt(0)
	v_cvt_pk_bf16_f32 v64, v65, v64
	ds_read_b32 v65, v56 offset:7196
	ds_read_b32 v69, v56 offset:6168
	s_waitcnt lgkmcnt(0)
	v_cvt_pk_bf16_f32 v65, v69, v65
	ds_read_b32 v70, v58 offset:1028
	ds_read_b32 v71, v58
	v_ashrrev_i32_e32 v69, 31, v68
	v_lshlrev_b64 v[68:69], 12, v[68:69]
	v_lshl_add_u64 v[68:69], v[66:67], 0, v[68:69]
	global_store_dwordx4 v[68:69], v[62:65], off nt
	v_add_u32_e32 v68, s9, v57
	s_waitcnt lgkmcnt(0)
	v_cvt_pk_bf16_f32 v62, v71, v70
	ds_read_b32 v63, v58 offset:3084
	ds_read_b32 v64, v58 offset:2056
	s_waitcnt lgkmcnt(0)
	v_cvt_pk_bf16_f32 v63, v64, v63
	ds_read_b32 v64, v58 offset:5140
	ds_read_b32 v65, v58 offset:4112
	s_waitcnt lgkmcnt(0)
	v_cvt_pk_bf16_f32 v64, v65, v64
	ds_read_b32 v65, v58 offset:7196
	ds_read_b32 v69, v58 offset:6168
	s_waitcnt lgkmcnt(0)
	v_cvt_pk_bf16_f32 v65, v69, v65
	ds_read_b32 v70, v60 offset:1028
	ds_read_b32 v71, v60
	v_ashrrev_i32_e32 v69, 31, v68
	v_lshlrev_b64 v[68:69], 12, v[68:69]
	v_lshl_add_u64 v[68:69], v[66:67], 0, v[68:69]
	global_store_dwordx4 v[68:69], v[62:65], off nt
	v_add_u32_e32 v68, s9, v59
	s_mov_b32 s9, s8
	s_waitcnt lgkmcnt(0)
	v_cvt_pk_bf16_f32 v62, v71, v70
	ds_read_b32 v63, v60 offset:3084
	ds_read_b32 v64, v60 offset:2056
	s_waitcnt lgkmcnt(0)
	v_cvt_pk_bf16_f32 v63, v64, v63
	ds_read_b32 v64, v60 offset:5140
	ds_read_b32 v65, v60 offset:4112
	s_waitcnt lgkmcnt(0)
	v_cvt_pk_bf16_f32 v64, v65, v64
	ds_read_b32 v65, v60 offset:7196
	ds_read_b32 v69, v60 offset:6168
	s_waitcnt lgkmcnt(0)
	v_cvt_pk_bf16_f32 v65, v69, v65
	v_ashrrev_i32_e32 v69, 31, v68
	v_lshlrev_b64 v[68:69], 12, v[68:69]
	v_lshl_add_u64 v[66:67], v[66:67], 0, v[68:69]
	global_store_dwordx4 v[66:67], v[62:65], off nt
	s_cbranch_vccz .LBB0_96

; #define LAS __attribute__((address_space(3)))
; __device__ __forceinline__ unsigned cvt_pk_bf16(float lo, float hi) { unsigned r; asm volatile("v_cvt_pk_bf16_f32 %0, %1, %2" : "=v"(r) : "v"(lo), "v"(hi)); return r; }
; #define CVT_LOAD(jx) do { const int b_ = (jx) / per, r_ = (jx) - b_ * per, kt_ = r_ / tn, nt_ = r_ - kt_ * tn; \
;         const float* s_ = src + (size_t)b_ * sbs + (size_t)(kt_ * 64) * ldS + nt_ * 256; \
;         _Pragma("unroll") for (int q = 0; q < 8; ++q) v[q] = *(const float4*)(s_ + (size_t)(kr + 8 * q) * ldS + c4 * 4); } while (0)
;     ...
;         const int b = j / per, r = j - b * per, kt = r / tn, ntile = r - kt * tn;
;         __syncthreads();
; #pragma unroll
;         for (int q = 0; q < 8; ++q) { LAS float* tp = tile + (kr + 8 * q) * 257 + c4 * 4; tp[0] = v[q].x; tp[1] = v[q].y; tp[2] = v[q].z; tp[3] = v[q].w; }
;         if (j + G < total) CVT_LOAD(j + G);
;         __syncthreads();
;         bf16_t* dmat = dst + (size_t)b * dbs;
; #pragma unroll
;         for (int q = 0; q < 4; ++q) {
;             const int id = tid + NTHR * q, nr = id >> 3, kc = id & 7;
;             const int n = ntile * 256 + nr;
;             const int drow = (mode == 0) ? n : ((n >> 7) * 256 + (mode == 2 ? 128 : 0) + (n & 127));
;             const LAS float* tp = tile + (kc * 8) * 257 + nr;
;             u32x4 w; w.x = cvt_pk_bf16(tp[0], tp[257]); w.y = cvt_pk_bf16(tp[2 * 257], tp[3 * 257]); w.z = cvt_pk_bf16(tp[4 * 257], tp[5 * 257]); w.w = cvt_pk_bf16(tp[6 * 257], tp[7 * 257]);
;             if (nrimg) *(u32x4*)(dmat + ((size_t)(kt * 8 + kc) * nrimg + drow) * 8) = w;
;             else *(u32x4*)(dmat + (size_t)drow * K + kt * 64 + kc * 8) = w;
.LBB0_99:
	s_waitcnt lgkmcnt(0)
	s_barrier
	ds_read_b32 v62, v54 offset:1028
	ds_read_b32 v63, v54
	s_ashr_i32 s19, s18, 31
	s_waitcnt lgkmcnt(0)
	v_cvt_pk_bf16_f32 v62, v63, v62
	ds_read_b32 v63, v54 offset:3084
	ds_read_b32 v64, v54 offset:2056
	s_waitcnt lgkmcnt(0)
	v_cvt_pk_bf16_f32 v63, v64, v63
	ds_read_b32 v64, v54 offset:5140
	ds_read_b32 v65, v54 offset:4112
	s_lshr_b32 s19, s19, 24
	s_add_i32 s19, s18, s19
	s_and_b32 s19, s19, 0xffffff00
	s_sub_i32 s18, s18, s19
	s_bfe_u32 s19, s18, 0x3001c
	s_waitcnt lgkmcnt(0)
	v_cvt_pk_bf16_f32 v64, v65, v64
	ds_read_b32 v65, v54 offset:7196
	ds_read_b32 v69, v54 offset:6168
	s_add_i32 s19, s18, s19
	s_sext_i32_i16 s19, s19
	s_ashr_i32 s19, s19, 3
	s_lshl_b32 s20, s19, 11
	s_lshl_b32 s18, s18, 8
	s_sub_i32 s20, s18, s20
	s_waitcnt lgkmcnt(0)
	v_cvt_pk_bf16_f32 v65, v69, v65
	ds_read_b32 v70, v56 offset:1028
	ds_read_b32 v71, v56
	s_lshl_b32 s18, s19, 6
	v_add_u32_e32 v68, s20, v1
	s_ashr_i32 s19, s18, 31
	v_ashrrev_i32_e32 v69, 31, v68
	v_lshl_add_u64 v[66:67], s[18:19], 1, v[52:53]
	v_lshlrev_b64 v[68:69], 12, v[68:69]
	v_lshl_add_u64 v[68:69], v[66:67], 0, v[68:69]
	global_store_dwordx4 v[68:69], v[62:65], off nt
	v_add_u32_e32 v68, s20, v55
	s_andn2_b64 vcc, exec, s[14:15]
	s_waitcnt lgkmcnt(0)
	v_cvt_pk_bf16_f32 v62, v71, v70
	ds_read_b32 v63, v56 offset:3084
	ds_read_b32 v64, v56 offset:2056
	s_waitcnt lgkmcnt(0)
	v_cvt_pk_bf16_f32 v63, v64, v63
	ds_read_b32 v64, v56 offset:5140
	ds_read_b32 v65, v56 offset:4112
	s_waitcnt lgkmcnt(0)
	v_cvt_pk_bf16_f32 v64, v65, v64
	ds_read_b32 v65, v56 offset:7196
	ds_read_b32 v69, v56 offset:6168
	s_waitcnt lgkmcnt(0)
	v_cvt_pk_bf16_f32 v65, v69, v65
	ds_read_b32 v70, v58 offset:1028
	ds_read_b32 v71, v58
	v_ashrrev_i32_e32 v69, 31, v68
	v_lshlrev_b64 v[68:69], 12, v[68:69]
	v_lshl_add_u64 v[68:69], v[66:67], 0, v[68:69]
	global_store_dwordx4 v[68:69], v[62:65], off nt
	v_add_u32_e32 v68, s20, v57
	s_mov_b32 s18, s17
	s_waitcnt lgkmcnt(0)
	v_cvt_pk_bf16_f32 v62, v71, v70
	ds_read_b32 v63, v58 offset:3084
	ds_read_b32 v64, v58 offset:2056
	s_waitcnt lgkmcnt(0)
	v_cvt_pk_bf16_f32 v63, v64, v63
	ds_read_b32 v64, v58 offset:5140
	ds_read_b32 v65, v58 offset:4112
	s_waitcnt lgkmcnt(0)
	v_cvt_pk_bf16_f32 v64, v65, v64
	ds_read_b32 v65, v58 offset:7196
	ds_read_b32 v69, v58 offset:6168
	s_waitcnt lgkmcnt(0)
	v_cvt_pk_bf16_f32 v65, v69, v65
	ds_read_b32 v70, v60 offset:1028
	ds_read_b32 v71, v60
	v_ashrrev_i32_e32 v69, 31, v68
	v_lshlrev_b64 v[68:69], 12, v[68:69]
	v_lshl_add_u64 v[68:69], v[66:67], 0, v[68:69]
	global_store_dwordx4 v[68:69], v[62:65], off nt
	v_add_u32_e32 v68, s20, v59
	s_waitcnt lgkmcnt(0)
	v_cvt_pk_bf16_f32 v62, v71, v70
	ds_read_b32 v63, v60 offset:3084
	ds_read_b32 v64, v60 offset:2056
	s_waitcnt lgkmcnt(0)
	v_cvt_pk_bf16_f32 v63, v64, v63
	ds_read_b32 v64, v60 offset:5140
	ds_read_b32 v65, v60 offset:4112
	s_waitcnt lgkmcnt(0)
	v_cvt_pk_bf16_f32 v64, v65, v64
	ds_read_b32 v65, v60 offset:7196
	ds_read_b32 v69, v60 offset:6168
	s_waitcnt lgkmcnt(0)
	v_cvt_pk_bf16_f32 v65, v69, v65
	v_ashrrev_i32_e32 v69, 31, v68
	v_lshlrev_b64 v[68:69], 12, v[68:69]
	v_lshl_add_u64 v[66:67], v[66:67], 0, v[68:69]
	global_store_dwordx4 v[66:67], v[62:65], off nt
	s_cbranch_vccz .LBB0_102

; #define LAS __attribute__((address_space(3)))
; __device__ __forceinline__ unsigned cvt_pk_bf16(float lo, float hi) { unsigned r; asm volatile("v_cvt_pk_bf16_f32 %0, %1, %2" : "=v"(r) : "v"(lo), "v"(hi)); return r; }
; #define CVT_LOAD(jx) do { const int b_ = (jx) / per, r_ = (jx) - b_ * per, kt_ = r_ / tn, nt_ = r_ - kt_ * tn; \
;         const float* s_ = src + (size_t)b_ * sbs + (size_t)(kt_ * 64) * ldS + nt_ * 256; \
;         _Pragma("unroll") for (int q = 0; q < 8; ++q) v[q] = *(const float4*)(s_ + (size_t)(kr + 8 * q) * ldS + c4 * 4); } while (0)
;     ...
;         const int b = j / per, r = j - b * per, kt = r / tn, ntile = r - kt * tn;
;         __syncthreads();
; #pragma unroll
;         for (int q = 0; q < 8; ++q) { LAS float* tp = tile + (kr + 8 * q) * 257 + c4 * 4; tp[0] = v[q].x; tp[1] = v[q].y; tp[2] = v[q].z; tp[3] = v[q].w; }
;         if (j + G < total) CVT_LOAD(j + G);
;         __syncthreads();
;         bf16_t* dmat = dst + (size_t)b * dbs;
; #pragma unroll
;         for (int q = 0; q < 4; ++q) {
;             const int id = tid + NTHR * q, nr = id >> 3, kc = id & 7;
;             const int n = ntile * 256 + nr;
;             const int drow = (mode == 0) ? n : ((n >> 7) * 256 + (mode == 2 ? 128 : 0) + (n & 127));
;             const LAS float* tp = tile + (kc * 8) * 257 + nr;
;             u32x4 w; w.x = cvt_pk_bf16(tp[0], tp[257]); w.y = cvt_pk_bf16(tp[2 * 257], tp[3 * 257]); w.z = cvt_pk_bf16(tp[4 * 257], tp[5 * 257]); w.w = cvt_pk_bf16(tp[6 * 257], tp[7 * 257]);
;             if (nrimg) *(u32x4*)(dmat + ((size_t)(kt * 8 + kc) * nrimg + drow) * 8) = w;
;             else *(u32x4*)(dmat + (size_t)drow * K + kt * 64 + kc * 8) = w;
.LBB0_104:
	s_waitcnt lgkmcnt(0)
	s_barrier
	ds_read_b32 v62, v54 offset:1028
	ds_read_b32 v63, v54
	s_mul_hi_i32 s13, s11, 0x2aaaaaab
	s_waitcnt lgkmcnt(0)
	v_cvt_pk_bf16_f32 v62, v63, v62
	ds_read_b32 v63, v54 offset:3084
	ds_read_b32 v64, v54 offset:2056
	s_waitcnt lgkmcnt(0)
	v_cvt_pk_bf16_f32 v63, v64, v63
	ds_read_b32 v64, v54 offset:5140
	ds_read_b32 v65, v54 offset:4112
	s_lshr_b32 s14, s13, 31
	s_lshr_b32 s13, s13, 7
	s_add_i32 s13, s13, s14
	s_mulk_i32 s13, 0x300
	s_sub_i32 s11, s11, s13
	s_mul_i32 s13, s11, 0x2aab
	s_waitcnt lgkmcnt(0)
	v_cvt_pk_bf16_f32 v64, v65, v64
	ds_read_b32 v65, v54 offset:7196
	ds_read_b32 v69, v54 offset:6168
	s_lshr_b32 s14, s13, 31
	s_ashr_i32 s13, s13, 18
	s_add_i32 s13, s13, s14
	s_mul_i32 s14, s13, 0xffffffe8
	s_add_i32 s14, s14, s11
	s_lshl_b32 s11, s14, 8
	s_waitcnt lgkmcnt(0)
	v_cvt_pk_bf16_f32 v65, v69, v65
	ds_read_b32 v70, v56 offset:1028
	ds_read_b32 v71, v56
	s_lshl_b32 s14, s13, 6
	v_add_u32_e32 v68, s11, v1
	s_ashr_i32 s15, s14, 31
	v_ashrrev_i32_e32 v69, 31, v68
	v_lshl_add_u64 v[66:67], s[14:15], 1, v[52:53]
	v_lshlrev_b64 v[68:69], 12, v[68:69]
	v_lshl_add_u64 v[68:69], v[66:67], 0, v[68:69]
	global_store_dwordx4 v[68:69], v[62:65], off nt
	v_add_u32_e32 v68, s11, v55
	s_andn2_b64 vcc, exec, s[0:1]
	s_waitcnt lgkmcnt(0)
	v_cvt_pk_bf16_f32 v62, v71, v70
	ds_read_b32 v63, v56 offset:3084
	ds_read_b32 v64, v56 offset:2056
	s_waitcnt lgkmcnt(0)
	v_cvt_pk_bf16_f32 v63, v64, v63
	ds_read_b32 v64, v56 offset:5140
	ds_read_b32 v65, v56 offset:4112
	s_waitcnt lgkmcnt(0)
	v_cvt_pk_bf16_f32 v64, v65, v64
	ds_read_b32 v65, v56 offset:7196
	ds_read_b32 v69, v56 offset:6168
	s_waitcnt lgkmcnt(0)
	v_cvt_pk_bf16_f32 v65, v69, v65
	ds_read_b32 v70, v58 offset:1028
	ds_read_b32 v71, v58
	v_ashrrev_i32_e32 v69, 31, v68
	v_lshlrev_b64 v[68:69], 12, v[68:69]
	v_lshl_add_u64 v[68:69], v[66:67], 0, v[68:69]
	global_store_dwordx4 v[68:69], v[62:65], off nt
	v_add_u32_e32 v68, s11, v57
	s_waitcnt lgkmcnt(0)
	v_cvt_pk_bf16_f32 v62, v71, v70
	ds_read_b32 v63, v58 offset:3084
	ds_read_b32 v64, v58 offset:2056
	s_waitcnt lgkmcnt(0)
	v_cvt_pk_bf16_f32 v63, v64, v63
	ds_read_b32 v64, v58 offset:5140
	ds_read_b32 v65, v58 offset:4112
	s_waitcnt lgkmcnt(0)
	v_cvt_pk_bf16_f32 v64, v65, v64
	ds_read_b32 v65, v58 offset:7196
	ds_read_b32 v69, v58 offset:6168
	s_waitcnt lgkmcnt(0)
	v_cvt_pk_bf16_f32 v65, v69, v65
	ds_read_b32 v70, v60 offset:1028
	ds_read_b32 v71, v60
	v_ashrrev_i32_e32 v69, 31, v68
	v_lshlrev_b64 v[68:69], 12, v[68:69]
	v_lshl_add_u64 v[68:69], v[66:67], 0, v[68:69]
	global_store_dwordx4 v[68:69], v[62:65], off nt
	v_add_u32_e32 v68, s11, v59
	s_mov_b32 s11, s10
	s_waitcnt lgkmcnt(0)
	v_cvt_pk_bf16_f32 v62, v71, v70
	ds_read_b32 v63, v60 offset:3084
	ds_read_b32 v64, v60 offset:2056
	s_waitcnt lgkmcnt(0)
	v_cvt_pk_bf16_f32 v63, v64, v63
	ds_read_b32 v64, v60 offset:5140
	ds_read_b32 v65, v60 offset:4112
	s_waitcnt lgkmcnt(0)
	v_cvt_pk_bf16_f32 v64, v65, v64
	ds_read_b32 v65, v60 offset:7196
	ds_read_b32 v69, v60 offset:6168
	s_waitcnt lgkmcnt(0)
	v_cvt_pk_bf16_f32 v65, v69, v65
	v_ashrrev_i32_e32 v69, 31, v68
	v_lshlrev_b64 v[68:69], 12, v[68:69]
	v_lshl_add_u64 v[66:67], v[66:67], 0, v[68:69]
	global_store_dwordx4 v[66:67], v[62:65], off nt
	s_cbranch_vccz .LBB0_107

; #define LAS __attribute__((address_space(3)))
; __device__ __forceinline__ unsigned cvt_pk_bf16(float lo, float hi) { unsigned r; asm volatile("v_cvt_pk_bf16_f32 %0, %1, %2" : "=v"(r) : "v"(lo), "v"(hi)); return r; }
; #define CVT_LOAD(jx) do { const int b_ = (jx) / per, r_ = (jx) - b_ * per, kt_ = r_ / tn, nt_ = r_ - kt_ * tn; \
;         const float* s_ = src + (size_t)b_ * sbs + (size_t)(kt_ * 64) * ldS + nt_ * 256; \
;         _Pragma("unroll") for (int q = 0; q < 8; ++q) v[q] = *(const float4*)(s_ + (size_t)(kr + 8 * q) * ldS + c4 * 4); } while (0)
;     ...
;         const int b = j / per, r = j - b * per, kt = r / tn, ntile = r - kt * tn;
;         __syncthreads();
; #pragma unroll
;         for (int q = 0; q < 8; ++q) { LAS float* tp = tile + (kr + 8 * q) * 257 + c4 * 4; tp[0] = v[q].x; tp[1] = v[q].y; tp[2] = v[q].z; tp[3] = v[q].w; }
;         if (j + G < total) CVT_LOAD(j + G);
;         __syncthreads();
;         bf16_t* dmat = dst + (size_t)b * dbs;
; #pragma unroll
;         for (int q = 0; q < 4; ++q) {
;             const int id = tid + NTHR * q, nr = id >> 3, kc = id & 7;
;             const int n = ntile * 256 + nr;
;             const int drow = (mode == 0) ? n : ((n >> 7) * 256 + (mode == 2 ? 128 : 0) + (n & 127));
;             const LAS float* tp = tile + (kc * 8) * 257 + nr;
;             u32x4 w; w.x = cvt_pk_bf16(tp[0], tp[257]); w.y = cvt_pk_bf16(tp[2 * 257], tp[3 * 257]); w.z = cvt_pk_bf16(tp[4 * 257], tp[5 * 257]); w.w = cvt_pk_bf16(tp[6 * 257], tp[7 * 257]);
;             if (nrimg) *(u32x4*)(dmat + ((size_t)(kt * 8 + kc) * nrimg + drow) * 8) = w;
;             else *(u32x4*)(dmat + (size_t)drow * K + kt * 64 + kc * 8) = w;
.LBB0_109:
	s_waitcnt lgkmcnt(0)
	s_barrier
	ds_read_b32 v62, v54 offset:1028
	ds_read_b32 v63, v54
	s_ashr_i32 s6, s5, 31
	s_waitcnt lgkmcnt(0)
	v_cvt_pk_bf16_f32 v62, v63, v62
	ds_read_b32 v63, v54 offset:3084
	ds_read_b32 v64, v54 offset:2056
	s_waitcnt lgkmcnt(0)
	v_cvt_pk_bf16_f32 v63, v64, v63
	ds_read_b32 v64, v54 offset:5140
	ds_read_b32 v65, v54 offset:4112
	s_lshr_b32 s6, s6, 24
	s_add_i32 s6, s5, s6
	s_and_b32 s6, s6, 0xffffff00
	s_sub_i32 s5, s5, s6
	s_bfe_u32 s6, s5, 0x3001c
	s_waitcnt lgkmcnt(0)
	v_cvt_pk_bf16_f32 v64, v65, v64
	ds_read_b32 v65, v54 offset:7196
	ds_read_b32 v69, v54 offset:6168
	s_add_i32 s6, s5, s6
	s_sext_i32_i16 s6, s6
	s_ashr_i32 s6, s6, 3
	s_lshl_b32 s7, s6, 11
	s_lshl_b32 s5, s5, 8
	s_sub_i32 s5, s5, s7
	s_waitcnt lgkmcnt(0)
	v_cvt_pk_bf16_f32 v65, v69, v65
	ds_read_b32 v70, v56 offset:1028
	ds_read_b32 v71, v56
	s_lshl_b32 s6, s6, 6
	v_add_u32_e32 v68, s5, v1
	s_ashr_i32 s7, s6, 31
	v_ashrrev_i32_e32 v69, 31, v68
	v_lshl_add_u64 v[66:67], s[6:7], 1, v[52:53]
	v_lshlrev_b64 v[68:69], 12, v[68:69]
	v_lshl_add_u64 v[68:69], v[66:67], 0, v[68:69]
	global_store_dwordx4 v[68:69], v[62:65], off nt
	v_add_u32_e32 v68, s5, v55
	s_andn2_b64 vcc, exec, s[2:3]
	s_waitcnt lgkmcnt(0)
	v_cvt_pk_bf16_f32 v62, v71, v70
	ds_read_b32 v63, v56 offset:3084
	ds_read_b32 v64, v56 offset:2056
	s_waitcnt lgkmcnt(0)
	v_cvt_pk_bf16_f32 v63, v64, v63
	ds_read_b32 v64, v56 offset:5140
	ds_read_b32 v65, v56 offset:4112
	s_waitcnt lgkmcnt(0)
	v_cvt_pk_bf16_f32 v64, v65, v64
	ds_read_b32 v65, v56 offset:7196
	ds_read_b32 v69, v56 offset:6168
	s_waitcnt lgkmcnt(0)
	v_cvt_pk_bf16_f32 v65, v69, v65
	ds_read_b32 v70, v58 offset:1028
	ds_read_b32 v71, v58
	v_ashrrev_i32_e32 v69, 31, v68
	v_lshlrev_b64 v[68:69], 12, v[68:69]
	v_lshl_add_u64 v[68:69], v[66:67], 0, v[68:69]
	global_store_dwordx4 v[68:69], v[62:65], off nt
	v_add_u32_e32 v68, s5, v57
	s_waitcnt lgkmcnt(0)
	v_cvt_pk_bf16_f32 v62, v71, v70
	ds_read_b32 v63, v58 offset:3084
	ds_read_b32 v64, v58 offset:2056
	s_waitcnt lgkmcnt(0)
	v_cvt_pk_bf16_f32 v63, v64, v63
	ds_read_b32 v64, v58 offset:5140
	ds_read_b32 v65, v58 offset:4112
	s_waitcnt lgkmcnt(0)
	v_cvt_pk_bf16_f32 v64, v65, v64
	ds_read_b32 v65, v58 offset:7196
	ds_read_b32 v69, v58 offset:6168
	s_waitcnt lgkmcnt(0)
	v_cvt_pk_bf16_f32 v65, v69, v65
	ds_read_b32 v70, v60 offset:1028
	ds_read_b32 v71, v60
	v_ashrrev_i32_e32 v69, 31, v68
	v_lshlrev_b64 v[68:69], 12, v[68:69]
	v_lshl_add_u64 v[68:69], v[66:67], 0, v[68:69]
	global_store_dwordx4 v[68:69], v[62:65], off nt
	v_add_u32_e32 v68, s5, v59
	s_mov_b32 s5, s4
	s_waitcnt lgkmcnt(0)
	v_cvt_pk_bf16_f32 v62, v71, v70
	ds_read_b32 v63, v60 offset:3084
	ds_read_b32 v64, v60 offset:2056
	s_waitcnt lgkmcnt(0)
	v_cvt_pk_bf16_f32 v63, v64, v63
	ds_read_b32 v64, v60 offset:5140
	ds_read_b32 v65, v60 offset:4112
	s_waitcnt lgkmcnt(0)
	v_cvt_pk_bf16_f32 v64, v65, v64
	ds_read_b32 v65, v60 offset:7196
	ds_read_b32 v69, v60 offset:6168
	s_waitcnt lgkmcnt(0)
	v_cvt_pk_bf16_f32 v65, v69, v65
	v_ashrrev_i32_e32 v69, 31, v68
	v_lshlrev_b64 v[68:69], 12, v[68:69]
	v_lshl_add_u64 v[66:67], v[66:67], 0, v[68:69]
	global_store_dwordx4 v[66:67], v[62:65], off nt
	s_cbranch_vccz .LBB0_112

; #define LAS __attribute__((address_space(3)))
; __device__ __forceinline__ unsigned cvt_pk_bf16(float lo, float hi) { unsigned r; asm volatile("v_cvt_pk_bf16_f32 %0, %1, %2" : "=v"(r) : "v"(lo), "v"(hi)); return r; }
; #define CVT_LOAD(jx) do { const int b_ = (jx) / per, r_ = (jx) - b_ * per, kt_ = r_ / tn, nt_ = r_ - kt_ * tn; \
;         const float* s_ = src + (size_t)b_ * sbs + (size_t)(kt_ * 64) * ldS + nt_ * 256; \
;         _Pragma("unroll") for (int q = 0; q < 8; ++q) v[q] = *(const float4*)(s_ + (size_t)(kr + 8 * q) * ldS + c4 * 4); } while (0)
;     ...
;         const int b = j / per, r = j - b * per, kt = r / tn, ntile = r - kt * tn;
;         __syncthreads();
; #pragma unroll
;         for (int q = 0; q < 8; ++q) { LAS float* tp = tile + (kr + 8 * q) * 257 + c4 * 4; tp[0] = v[q].x; tp[1] = v[q].y; tp[2] = v[q].z; tp[3] = v[q].w; }
;         if (j + G < total) CVT_LOAD(j + G);
;         __syncthreads();
;         bf16_t* dmat = dst + (size_t)b * dbs;
; #pragma unroll
;         for (int q = 0; q < 4; ++q) {
;             const int id = tid + NTHR * q, nr = id >> 3, kc = id & 7;
;             const int n = ntile * 256 + nr;
;             const int drow = (mode == 0) ? n : ((n >> 7) * 256 + (mode == 2 ? 128 : 0) + (n & 127));
;             const LAS float* tp = tile + (kc * 8) * 257 + nr;
;             u32x4 w; w.x = cvt_pk_bf16(tp[0], tp[257]); w.y = cvt_pk_bf16(tp[2 * 257], tp[3 * 257]); w.z = cvt_pk_bf16(tp[4 * 257], tp[5 * 257]); w.w = cvt_pk_bf16(tp[6 * 257], tp[7 * 257]);
;             if (nrimg) *(u32x4*)(dmat + ((size_t)(kt * 8 + kc) * nrimg + drow) * 8) = w;
;             else *(u32x4*)(dmat + (size_t)drow * K + kt * 64 + kc * 8) = w;
.LBB0_116:
	s_waitcnt lgkmcnt(0)
	s_barrier
	ds_read_b32 v65, v54 offset:1028
	ds_read_b32 v66, v54
	s_ashr_i32 s34, s33, 31
	s_waitcnt lgkmcnt(0)
	v_cvt_pk_bf16_f32 v66, v66, v65
	ds_read_b32 v65, v54 offset:3084
	ds_read_b32 v67, v54 offset:2056
	s_lshr_b32 s34, s34, 26
	s_add_i32 s34, s33, s34
	s_waitcnt lgkmcnt(0)
	v_cvt_pk_bf16_f32 v67, v67, v65
	ds_read_b32 v65, v54 offset:5140
	ds_read_b32 v68, v54 offset:4112
	s_andn2_b32 s34, s34, 63
	s_sub_i32 s33, s33, s34
	s_bfe_u32 s34, s33, 0x10007
	s_add_i32 s34, s33, s34
	s_bfe_i32 s34, s34, 0x80000
	s_waitcnt lgkmcnt(0)
	v_cvt_pk_bf16_f32 v68, v68, v65
	ds_read_b32 v65, v54 offset:7196
	ds_read_b32 v69, v54 offset:6168
	s_sext_i32_i16 s34, s34
	s_ashr_i32 s34, s34, 1
	s_lshl_b32 s35, s34, 9
	s_lshl_b32 s33, s33, 8
	s_sub_i32 s33, s33, s35
	v_lshl_or_b32 v70, s34, 3, v1
	v_add_lshl_u32 v72, s33, v52, 1
	s_waitcnt lgkmcnt(0)
	v_cvt_pk_bf16_f32 v69, v69, v65
	ds_read_b32 v65, v57 offset:1028
	ds_read_b32 v74, v57
	v_ashrrev_i32_e32 v71, 31, v70
	v_and_or_b32 v72, v72, s26, v53
	v_lshlrev_b64 v[70:71], 10, v[70:71]
	v_ashrrev_i32_e32 v73, 31, v72
	v_lshl_add_u64 v[72:73], v[70:71], 0, v[72:73]
	v_lshl_add_u64 v[72:73], v[72:73], 4, s[20:21]
	global_store_dwordx4 v[72:73], v[66:69], off nt
	v_add_lshl_u32 v72, s33, v55, 1
	v_and_or_b32 v72, v72, s26, v56
	s_waitcnt lgkmcnt(0)
	v_cvt_pk_bf16_f32 v66, v74, v65
	ds_read_b32 v65, v57 offset:3084
	ds_read_b32 v67, v57 offset:2056
	s_waitcnt lgkmcnt(0)
	v_cvt_pk_bf16_f32 v67, v67, v65
	ds_read_b32 v65, v57 offset:5140
	ds_read_b32 v68, v57 offset:4112
	s_waitcnt lgkmcnt(0)
	v_cvt_pk_bf16_f32 v68, v68, v65
	ds_read_b32 v65, v57 offset:7196
	ds_read_b32 v69, v57 offset:6168
	s_waitcnt lgkmcnt(0)
	v_cvt_pk_bf16_f32 v69, v69, v65
	ds_read_b32 v65, v60 offset:1028
	ds_read_b32 v74, v60
	v_ashrrev_i32_e32 v73, 31, v72
	v_lshl_add_u64 v[72:73], v[70:71], 0, v[72:73]
	v_lshl_add_u64 v[72:73], v[72:73], 4, s[20:21]
	global_store_dwordx4 v[72:73], v[66:69], off nt
	v_add_lshl_u32 v72, s33, v58, 1
	v_and_or_b32 v72, v72, s26, v59
	s_waitcnt lgkmcnt(0)
	v_cvt_pk_bf16_f32 v66, v74, v65
	ds_read_b32 v65, v60 offset:3084
	ds_read_b32 v67, v60 offset:2056
	s_waitcnt lgkmcnt(0)
	v_cvt_pk_bf16_f32 v67, v67, v65
	ds_read_b32 v65, v60 offset:5140
	ds_read_b32 v68, v60 offset:4112
	s_waitcnt lgkmcnt(0)
	v_cvt_pk_bf16_f32 v68, v68, v65
	ds_read_b32 v65, v60 offset:7196
	ds_read_b32 v69, v60 offset:6168
	s_waitcnt lgkmcnt(0)
	v_cvt_pk_bf16_f32 v69, v69, v65
	ds_read_b32 v65, v63 offset:1028
	ds_read_b32 v74, v63
	v_ashrrev_i32_e32 v73, 31, v72
	v_lshl_add_u64 v[72:73], v[70:71], 0, v[72:73]
	v_lshl_add_u64 v[72:73], v[72:73], 4, s[20:21]
	global_store_dwordx4 v[72:73], v[66:69], off nt
	v_add_lshl_u32 v72, s33, v61, 1
	v_and_or_b32 v72, v72, s26, v62
	s_waitcnt lgkmcnt(0)
	v_cvt_pk_bf16_f32 v66, v74, v65
	ds_read_b32 v65, v63 offset:3084
	ds_read_b32 v67, v63 offset:2056
	s_waitcnt lgkmcnt(0)
	v_cvt_pk_bf16_f32 v67, v67, v65
	ds_read_b32 v65, v63 offset:5140
	ds_read_b32 v68, v63 offset:4112
	s_waitcnt lgkmcnt(0)
	v_cvt_pk_bf16_f32 v68, v68, v65
	ds_read_b32 v65, v63 offset:7196
	ds_read_b32 v69, v63 offset:6168
	v_ashrrev_i32_e32 v73, 31, v72
	v_lshl_add_u64 v[70:71], v[70:71], 0, v[72:73]
	v_lshl_add_u64 v[70:71], v[70:71], 4, s[20:21]
	s_andn2_b64 vcc, exec, s[24:25]
	s_mov_b32 s33, s31
	s_waitcnt lgkmcnt(0)
	v_cvt_pk_bf16_f32 v69, v69, v65
	global_store_dwordx4 v[70:71], v[66:69], off nt
	s_cbranch_vccz .LBB0_119

; #define LAS __attribute__((address_space(3)))
; __device__ __forceinline__ unsigned cvt_pk_bf16(float lo, float hi) { unsigned r; asm volatile("v_cvt_pk_bf16_f32 %0, %1, %2" : "=v"(r) : "v"(lo), "v"(hi)); return r; }
; #define CVT_LOAD(jx) do { const int b_ = (jx) / per, r_ = (jx) - b_ * per, kt_ = r_ / tn, nt_ = r_ - kt_ * tn; \
;         const float* s_ = src + (size_t)b_ * sbs + (size_t)(kt_ * 64) * ldS + nt_ * 256; \
;         _Pragma("unroll") for (int q = 0; q < 8; ++q) v[q] = *(const float4*)(s_ + (size_t)(kr + 8 * q) * ldS + c4 * 4); } while (0)
;     ...
;         const int b = j / per, r = j - b * per, kt = r / tn, ntile = r - kt * tn;
;         __syncthreads();
; #pragma unroll
;         for (int q = 0; q < 8; ++q) { LAS float* tp = tile + (kr + 8 * q) * 257 + c4 * 4; tp[0] = v[q].x; tp[1] = v[q].y; tp[2] = v[q].z; tp[3] = v[q].w; }
;         if (j + G < total) CVT_LOAD(j + G);
;         __syncthreads();
;         bf16_t* dmat = dst + (size_t)b * dbs;
; #pragma unroll
;         for (int q = 0; q < 4; ++q) {
;             const int id = tid + NTHR * q, nr = id >> 3, kc = id & 7;
;             const int n = ntile * 256 + nr;
;             const int drow = (mode == 0) ? n : ((n >> 7) * 256 + (mode == 2 ? 128 : 0) + (n & 127));
;             const LAS float* tp = tile + (kc * 8) * 257 + nr;
;             u32x4 w; w.x = cvt_pk_bf16(tp[0], tp[257]); w.y = cvt_pk_bf16(tp[2 * 257], tp[3 * 257]); w.z = cvt_pk_bf16(tp[4 * 257], tp[5 * 257]); w.w = cvt_pk_bf16(tp[6 * 257], tp[7 * 257]);
;             if (nrimg) *(u32x4*)(dmat + ((size_t)(kt * 8 + kc) * nrimg + drow) * 8) = w;
;             else *(u32x4*)(dmat + (size_t)drow * K + kt * 64 + kc * 8) = w;
.LBB0_121:
	s_waitcnt lgkmcnt(0)
	s_barrier
	ds_read_b32 v65, v53 offset:1028
	ds_read_b32 v66, v53
	s_ashr_i32 s31, s30, 31
	s_waitcnt lgkmcnt(0)
	v_cvt_pk_bf16_f32 v66, v66, v65
	ds_read_b32 v65, v53 offset:3084
	ds_read_b32 v67, v53 offset:2056
	s_lshr_b32 s31, s31, 26
	s_add_i32 s31, s30, s31
	s_waitcnt lgkmcnt(0)
	v_cvt_pk_bf16_f32 v67, v67, v65
	ds_read_b32 v65, v53 offset:5140
	ds_read_b32 v68, v53 offset:4112
	s_andn2_b32 s31, s31, 63
	s_sub_i32 s30, s30, s31
	s_bfe_u32 s31, s30, 0x10007
	s_add_i32 s31, s30, s31
	s_bfe_i32 s31, s31, 0x80000
	s_waitcnt lgkmcnt(0)
	v_cvt_pk_bf16_f32 v68, v68, v65
	ds_read_b32 v65, v53 offset:7196
	ds_read_b32 v69, v53 offset:6168
	s_sext_i32_i16 s31, s31
	s_ashr_i32 s31, s31, 1
	s_lshl_b32 s33, s31, 9
	s_lshl_b32 s30, s30, 8
	s_sub_i32 s30, s30, s33
	v_lshl_or_b32 v70, s31, 3, v1
	v_add_lshl_u32 v72, s30, v52, 1
	s_waitcnt lgkmcnt(0)
	v_cvt_pk_bf16_f32 v69, v69, v65
	ds_read_b32 v65, v55 offset:1028
	ds_read_b32 v74, v55
	v_ashrrev_i32_e32 v71, 31, v70
	v_and_or_b32 v72, v72, s26, v60
	v_lshlrev_b64 v[70:71], 10, v[70:71]
	v_ashrrev_i32_e32 v73, 31, v72
	v_lshl_add_u64 v[72:73], v[70:71], 0, v[72:73]
	v_lshl_add_u64 v[72:73], v[72:73], 4, s[20:21]
	global_store_dwordx4 v[72:73], v[66:69], off nt
	v_add_lshl_u32 v72, s30, v54, 1
	v_and_or_b32 v72, v72, s26, v61
	s_waitcnt lgkmcnt(0)
	v_cvt_pk_bf16_f32 v66, v74, v65
	ds_read_b32 v65, v55 offset:3084
	ds_read_b32 v67, v55 offset:2056
	s_waitcnt lgkmcnt(0)
	v_cvt_pk_bf16_f32 v67, v67, v65
	ds_read_b32 v65, v55 offset:5140
	ds_read_b32 v68, v55 offset:4112
	s_waitcnt lgkmcnt(0)
	v_cvt_pk_bf16_f32 v68, v68, v65
	ds_read_b32 v65, v55 offset:7196
	ds_read_b32 v69, v55 offset:6168
	s_waitcnt lgkmcnt(0)
	v_cvt_pk_bf16_f32 v69, v69, v65
	ds_read_b32 v65, v57 offset:1028
	ds_read_b32 v74, v57
	v_ashrrev_i32_e32 v73, 31, v72
	v_lshl_add_u64 v[72:73], v[70:71], 0, v[72:73]
	v_lshl_add_u64 v[72:73], v[72:73], 4, s[20:21]
	global_store_dwordx4 v[72:73], v[66:69], off nt
	v_add_lshl_u32 v72, s30, v56, 1
	v_and_or_b32 v72, v72, s26, v62
	s_waitcnt lgkmcnt(0)
	v_cvt_pk_bf16_f32 v66, v74, v65
	ds_read_b32 v65, v57 offset:3084
	ds_read_b32 v67, v57 offset:2056
	s_waitcnt lgkmcnt(0)
	v_cvt_pk_bf16_f32 v67, v67, v65
	ds_read_b32 v65, v57 offset:5140
	ds_read_b32 v68, v57 offset:4112
	s_waitcnt lgkmcnt(0)
	v_cvt_pk_bf16_f32 v68, v68, v65
	ds_read_b32 v65, v57 offset:7196
	ds_read_b32 v69, v57 offset:6168
	s_waitcnt lgkmcnt(0)
	v_cvt_pk_bf16_f32 v69, v69, v65
	ds_read_b32 v65, v59 offset:1028
	ds_read_b32 v74, v59
	v_ashrrev_i32_e32 v73, 31, v72
	v_lshl_add_u64 v[72:73], v[70:71], 0, v[72:73]
	v_lshl_add_u64 v[72:73], v[72:73], 4, s[20:21]
	global_store_dwordx4 v[72:73], v[66:69], off nt
	v_add_lshl_u32 v72, s30, v58, 1
	v_and_or_b32 v72, v72, s26, v63
	s_waitcnt lgkmcnt(0)
	v_cvt_pk_bf16_f32 v66, v74, v65
	ds_read_b32 v65, v59 offset:3084
	ds_read_b32 v67, v59 offset:2056
	s_waitcnt lgkmcnt(0)
	v_cvt_pk_bf16_f32 v67, v67, v65
	ds_read_b32 v65, v59 offset:5140
	ds_read_b32 v68, v59 offset:4112
	s_waitcnt lgkmcnt(0)
	v_cvt_pk_bf16_f32 v68, v68, v65
	ds_read_b32 v65, v59 offset:7196
	ds_read_b32 v69, v59 offset:6168
	v_ashrrev_i32_e32 v73, 31, v72
	v_lshl_add_u64 v[70:71], v[70:71], 0, v[72:73]
	v_lshl_add_u64 v[70:71], v[70:71], 4, s[20:21]
	s_andn2_b64 vcc, exec, s[22:23]
	s_mov_b32 s30, s29
	s_waitcnt lgkmcnt(0)
	v_cvt_pk_bf16_f32 v69, v69, v65
	global_store_dwordx4 v[70:71], v[66:69], off nt
	s_cbranch_vccz .LBB0_124

; #define LAS __attribute__((address_space(3)))
; __device__ __forceinline__ unsigned cvt_pk_bf16(float lo, float hi) { unsigned r; asm volatile("v_cvt_pk_bf16_f32 %0, %1, %2" : "=v"(r) : "v"(lo), "v"(hi)); return r; }
; #define CVT_LOAD(jx) do { const int b_ = (jx) / per, r_ = (jx) - b_ * per, kt_ = r_ / tn, nt_ = r_ - kt_ * tn; \
;         const float* s_ = src + (size_t)b_ * sbs + (size_t)(kt_ * 64) * ldS + nt_ * 256; \
;         _Pragma("unroll") for (int q = 0; q < 8; ++q) v[q] = *(const float4*)(s_ + (size_t)(kr + 8 * q) * ldS + c4 * 4); } while (0)
;     ...
;         const int b = j / per, r = j - b * per, kt = r / tn, ntile = r - kt * tn;
;         __syncthreads();
; #pragma unroll
;         for (int q = 0; q < 8; ++q) { LAS float* tp = tile + (kr + 8 * q) * 257 + c4 * 4; tp[0] = v[q].x; tp[1] = v[q].y; tp[2] = v[q].z; tp[3] = v[q].w; }
;         if (j + G < total) CVT_LOAD(j + G);
;         __syncthreads();
;         bf16_t* dmat = dst + (size_t)b * dbs;
; #pragma unroll
;         for (int q = 0; q < 4; ++q) {
;             const int id = tid + NTHR * q, nr = id >> 3, kc = id & 7;
;             const int n = ntile * 256 + nr;
;             const int drow = (mode == 0) ? n : ((n >> 7) * 256 + (mode == 2 ? 128 : 0) + (n & 127));
;             const LAS float* tp = tile + (kc * 8) * 257 + nr;
;             u32x4 w; w.x = cvt_pk_bf16(tp[0], tp[257]); w.y = cvt_pk_bf16(tp[2 * 257], tp[3 * 257]); w.z = cvt_pk_bf16(tp[4 * 257], tp[5 * 257]); w.w = cvt_pk_bf16(tp[6 * 257], tp[7 * 257]);
;             if (nrimg) *(u32x4*)(dmat + ((size_t)(kt * 8 + kc) * nrimg + drow) * 8) = w;
;             else *(u32x4*)(dmat + (size_t)drow * K + kt * 64 + kc * 8) = w;
.LBB0_126:
	s_waitcnt lgkmcnt(0)
	s_barrier
	ds_read_b32 v61, v53 offset:1028
	ds_read_b32 v62, v53
	s_ashr_i32 s24, s23, 31
	s_waitcnt lgkmcnt(0)
	v_cvt_pk_bf16_f32 v62, v62, v61
	ds_read_b32 v61, v53 offset:3084
	ds_read_b32 v63, v53 offset:2056
	s_lshr_b32 s24, s24, 26
	s_add_i32 s24, s23, s24
	s_waitcnt lgkmcnt(0)
	v_cvt_pk_bf16_f32 v63, v63, v61
	ds_read_b32 v61, v53 offset:5140
	ds_read_b32 v64, v53 offset:4112
	s_andn2_b32 s24, s24, 63
	s_sub_i32 s23, s23, s24
	s_bfe_i32 s24, s23, 0x80000
	s_bfe_u32 s24, s24, 0x3000c
	s_add_i32 s24, s23, s24
	s_waitcnt lgkmcnt(0)
	v_cvt_pk_bf16_f32 v64, v64, v61
	ds_read_b32 v61, v53 offset:7196
	ds_read_b32 v65, v53 offset:6168
	s_bfe_i32 s24, s24, 0x80000
	s_sext_i32_i16 s24, s24
	s_lshl_b32 s25, s24, 8
	s_and_b32 s25, s25, 0xfffff800
	s_lshl_b32 s23, s23, 8
	s_sub_i32 s23, s23, s25
	v_and_or_b32 v66, s24, -8, v1
	s_waitcnt lgkmcnt(0)
	v_cvt_pk_bf16_f32 v65, v65, v61
	ds_read_b32 v61, v55 offset:1028
	ds_read_b32 v70, v55
	v_ashrrev_i32_e32 v67, 31, v66
	v_add_u32_e32 v68, s23, v52
	v_lshlrev_b64 v[66:67], 11, v[66:67]
	v_ashrrev_i32_e32 v69, 31, v68
	v_lshl_add_u64 v[68:69], v[66:67], 0, v[68:69]
	v_lshl_add_u64 v[68:69], v[68:69], 4, s[14:15]
	global_store_dwordx4 v[68:69], v[62:65], off nt
	v_add_u32_e32 v68, s23, v54
	v_ashrrev_i32_e32 v69, 31, v68
	s_waitcnt lgkmcnt(0)
	v_cvt_pk_bf16_f32 v62, v70, v61
	ds_read_b32 v61, v55 offset:3084
	ds_read_b32 v63, v55 offset:2056
	s_waitcnt lgkmcnt(0)
	v_cvt_pk_bf16_f32 v63, v63, v61
	ds_read_b32 v61, v55 offset:5140
	ds_read_b32 v64, v55 offset:4112
	s_waitcnt lgkmcnt(0)
	v_cvt_pk_bf16_f32 v64, v64, v61
	ds_read_b32 v61, v55 offset:7196
	ds_read_b32 v65, v55 offset:6168
	s_waitcnt lgkmcnt(0)
	v_cvt_pk_bf16_f32 v65, v65, v61
	ds_read_b32 v61, v57 offset:1028
	ds_read_b32 v70, v57
	v_lshl_add_u64 v[68:69], v[66:67], 0, v[68:69]
	v_lshl_add_u64 v[68:69], v[68:69], 4, s[14:15]
	global_store_dwordx4 v[68:69], v[62:65], off nt
	v_add_u32_e32 v68, s23, v56
	v_ashrrev_i32_e32 v69, 31, v68
	s_waitcnt lgkmcnt(0)
	v_cvt_pk_bf16_f32 v62, v70, v61
	ds_read_b32 v61, v57 offset:3084
	ds_read_b32 v63, v57 offset:2056
	s_waitcnt lgkmcnt(0)
	v_cvt_pk_bf16_f32 v63, v63, v61
	ds_read_b32 v61, v57 offset:5140
	ds_read_b32 v64, v57 offset:4112
	s_waitcnt lgkmcnt(0)
	v_cvt_pk_bf16_f32 v64, v64, v61
	ds_read_b32 v61, v57 offset:7196
	ds_read_b32 v65, v57 offset:6168
	s_waitcnt lgkmcnt(0)
	v_cvt_pk_bf16_f32 v65, v65, v61
	ds_read_b32 v61, v59 offset:1028
	ds_read_b32 v70, v59
	v_lshl_add_u64 v[68:69], v[66:67], 0, v[68:69]
	v_lshl_add_u64 v[68:69], v[68:69], 4, s[14:15]
	global_store_dwordx4 v[68:69], v[62:65], off nt
	v_add_u32_e32 v68, s23, v58
	v_ashrrev_i32_e32 v69, 31, v68
	s_waitcnt lgkmcnt(0)
	v_cvt_pk_bf16_f32 v62, v70, v61
	ds_read_b32 v61, v59 offset:3084
	ds_read_b32 v63, v59 offset:2056
	s_waitcnt lgkmcnt(0)
	v_cvt_pk_bf16_f32 v63, v63, v61
	ds_read_b32 v61, v59 offset:5140
	ds_read_b32 v64, v59 offset:4112
	s_waitcnt lgkmcnt(0)
	v_cvt_pk_bf16_f32 v64, v64, v61
	ds_read_b32 v61, v59 offset:7196
	ds_read_b32 v65, v59 offset:6168
	v_lshl_add_u64 v[66:67], v[66:67], 0, v[68:69]
	v_lshl_add_u64 v[66:67], v[66:67], 4, s[14:15]
	s_andn2_b64 vcc, exec, s[18:19]
	s_mov_b32 s23, s22
	s_waitcnt lgkmcnt(0)
	v_cvt_pk_bf16_f32 v65, v65, v61
	global_store_dwordx4 v[66:67], v[62:65], off nt
	s_cbranch_vccz .LBB0_113

; __device__ __forceinline__ int tid_fresh() { int t = threadIdx.x; asm volatile("" : "+v"(t)); return t; }
; template <int MODE>
; __device__ __forceinline__ void combine_phase(LAS unsigned char* ldsb, int bid, int G, const float* x, const float* gf, const bf16_t* Y, const u32x2* rec,
;                                               float* xout, const float* ng, const float* sc, const float* sh, bf16_t* hbuf) {
;     ...
;     for (int rowi = bid * 16 + wave0 * 2; rowi < T; rowi += ((rowi & 1) ? (G * 16 - 1) : 1)) {
;         const int row = rowi;
;         const int lane = tid_fresh() & 63;
;         float a[4][8];
; #pragma unroll
;         for (int i = 0; i < 4; ++i)
; #pragma unroll
;             for (int q = 0; q < 8; ++q) a[i][q] = 0.f;
;         u32x2 rr[TOPK];
; #pragma unroll
;         for (int j = 0; j < TOPK; ++j) rr[j] = rec[row * TOPK + j];
;         float4 xr[4][2];
; #pragma unroll
;         for (int i = 0; i < 4; ++i) { const int c = lane * 8 + i * 512; xr[i][0] = *(const float4*)(x + (size_t)row * D + c); xr[i][1] = *(const float4*)(x + (size_t)row * D + c + 4); }
; #pragma unroll
;         for (int jb = 0; jb <= TOPK; jb += 8) {
;             u32x2 yv[7][4]; float wj[7];
; #pragma unroll
;             for (int jj = 0; jj < 7; ++jj) { const int j = jb + jj; if (j > TOPK) break;
;                 size_t slot = (size_t)SLOT_SH + row; wj[jj] = Y8_INV;
;                 if (j < TOPK) { const int e = (int)(rr[j].x >> 13), pos = (int)(rr[j].x & 8191u); wj[jj] = __uint_as_float(rr[j].y) * Y8_INV; slot = (size_t)tstart[e] * BM + pos; }
;                 const unsigned char* yp = (const unsigned char*)Y + slot * D + lane * 8;
; #pragma unroll
;                 for (int i = 0; i < 4; ++i) yv[jj][i] = *(const u32x2*)(yp + i * 512);
;             }
.LBB0_1958:
	v_mul_lo_u32 v2, v66, 6
	v_ashrrev_i32_e32 v3, 31, v2
	v_mov_b32_e32 v4, v0
	v_lshl_add_u64 v[2:3], v[2:3], 3, s[12:13]
	global_load_dwordx4 v[38:41], v[2:3], off
	global_load_dwordx4 v[44:47], v[2:3], off offset:16
	global_load_dwordx4 v[48:51], v[2:3], off offset:32
	v_cmp_lt_i32_e32 vcc, v79, v77
	v_and_b32_e32 v15, 1, v66
	v_ashrrev_i32_e32 v67, 31, v66
	v_cndmask_b32_e32 v5, v1, v79, vcc
	v_cmp_lt_i32_e32 vcc, v113, v77
	v_lshlrev_b64 v[6:7], 13, v[66:67]
	v_lshlrev_b64 v[8:9], 11, v[66:67]
	v_cndmask_b32_e32 v10, v1, v113, vcc
	v_cmp_lt_i32_e32 vcc, v114, v77
	v_lshlrev_b32_e32 v244, 2, v10
	v_mov_b32_e32 v35, v69
	v_cndmask_b32_e32 v11, v1, v114, vcc
	v_cmp_lt_i32_e32 vcc, v115, v77
	v_lshlrev_b32_e32 v245, 2, v11
	v_lshlrev_b32_e32 v11, 3, v4
	v_cndmask_b32_e32 v12, v1, v115, vcc
	v_cmp_lt_i32_e32 vcc, v116, v77
	v_and_b32_e32 v68, 0x1f8, v11
	v_lshl_add_u64 v[52:53], s[10:11], 0, v[68:69]
	v_cndmask_b32_e32 v13, v1, v116, vcc
	v_cmp_lt_i32_e32 vcc, v117, v77
	v_lshlrev_b32_e32 v34, 2, v68
	v_lshl_add_u64 v[2:3], v[52:53], 0, v[8:9]
	v_cndmask_b32_e32 v14, v1, v117, vcc
	v_cmp_eq_u32_e32 vcc, 1, v15
	v_mov_b32_e32 v37, v69
	v_mov_b32_e32 v43, v69
	v_cndmask_b32_e32 v10, 1, v119, vcc
	v_add_u32_e32 v66, v10, v66
	v_cmp_lt_i32_e32 vcc, s16, v66
	v_lshlrev_b32_e32 v67, 2, v5
	v_lshlrev_b32_e32 v248, 2, v14
	v_lshl_add_u64 v[4:5], s[68:69], 0, v[6:7]
	v_lshl_add_u64 v[14:15], s[2:3], 0, v[6:7]
	s_or_b64 s[4:5], vcc, s[4:5]
	v_or_b32_e32 v36, 0x1000, v34
	v_or_b32_e32 v42, 0x1800, v34
	v_add_co_u32_e32 v58, vcc, s14, v2
	v_lshl_add_u64 v[16:17], v[4:5], 0, v[34:35]
	v_lshl_add_u64 v[70:71], v[14:15], 0, v[34:35]
	v_lshl_add_u64 v[54:55], v[4:5], 0, v[36:37]
	v_lshl_add_u64 v[56:57], v[4:5], 0, v[42:43]
	v_addc_co_u32_e32 v59, vcc, 0, v3, vcc
	v_lshl_add_u64 v[74:75], v[14:15], 0, v[36:37]
	v_lshl_add_u64 v[72:73], v[14:15], 0, v[42:43]
	v_lshlrev_b32_e32 v246, 2, v12
	v_lshlrev_b32_e32 v247, 2, v13
	global_load_dwordx4 v[6:9], v[16:17], off offset:16
	global_load_dwordx4 v[18:21], v[16:17], off
	global_load_dwordx4 v[2:5], v[16:17], off offset:2064
	global_load_dwordx4 v[10:13], v[16:17], off offset:2048
	global_load_dwordx2 v[60:61], v[58:59], off
	global_load_dwordx2 v[62:63], v[58:59], off offset:512
	global_load_dwordx2 v[64:65], v[58:59], off offset:1024
	global_load_dwordx2 v[110:111], v[58:59], off offset:1536
	global_load_dwordx4 v[22:25], v[54:55], off offset:16
	global_load_dwordx4 v[30:33], v[54:55], off
	global_load_dwordx4 v[14:17], v[56:57], off offset:16
	global_load_dwordx4 v[26:29], v[56:57], off
	v_or_b32_e32 v132, 0x800, v34
	s_waitcnt vmcnt(14)
	v_mul_f32_e32 v152, 0x3d800000, v39
	v_lshrrev_b32_e32 v35, 11, v38
	v_lshlrev_b32_e32 v37, 11, v38
	v_lshrrev_b32_e32 v38, 11, v40
	v_lshlrev_b32_e32 v43, 11, v40
	s_waitcnt vmcnt(13)
	v_lshrrev_b32_e32 v39, 11, v44
	v_lshrrev_b32_e32 v40, 11, v46
	v_mul_f32_e32 v154, 0x3d800000, v41
	v_lshlrev_b32_e32 v54, 11, v44
	s_waitcnt vmcnt(12)
	v_lshrrev_b32_e32 v41, 11, v48
	v_lshrrev_b32_e32 v44, 11, v50
	v_and_b32_e32 v35, 0x1ffffc, v35
	v_and_b32_e32 v68, 0xfff800, v37
	v_and_b32_e32 v37, 0x1ffffc, v38
	v_and_b32_e32 v38, 0x1ffffc, v39
	v_and_b32_e32 v39, 0x1ffffc, v40
	v_and_b32_e32 v40, 0x1ffffc, v41
	v_and_b32_e32 v41, 0x1ffffc, v44
	v_add_u32_e32 v35, s7, v35
	v_add_u32_e32 v44, s7, v38
	v_add_u32_e32 v39, s7, v39
	v_mul_f32_e32 v156, 0x3d800000, v45
	v_lshlrev_b32_e32 v55, 11, v46
	v_lshlrev_b32_e32 v56, 11, v48
	v_lshlrev_b32_e32 v57, 11, v50
	v_add_u32_e32 v37, s7, v37
	v_add_u32_e32 v45, s7, v40
	v_add_u32_e32 v41, s7, v41
	ds_read_b32 v38, v35
	ds_read_b32 v40, v37
	ds_read_b32 v44, v44
	ds_read_b32 v46, v39
	ds_read_b32 v48, v45
	ds_read_b32 v50, v41
	s_waitcnt lgkmcnt(5)
	v_ashrrev_i32_e32 v39, 31, v38
	v_lshlrev_b64 v[38:39], 19, v[38:39]
	v_lshl_add_u64 v[38:39], v[52:53], 0, v[38:39]
	s_waitcnt lgkmcnt(4)
	v_ashrrev_i32_e32 v41, 31, v40
	v_lshl_add_u64 v[38:39], v[38:39], 0, v[68:69]
	v_lshlrev_b64 v[40:41], 19, v[40:41]
	global_load_dwordx2 v[158:159], v[38:39], off
	global_load_dwordx2 v[160:161], v[38:39], off offset:512
	global_load_dwordx2 v[162:163], v[38:39], off offset:1024
	global_load_dwordx2 v[164:165], v[38:39], off offset:1536
	v_lshl_add_u64 v[40:41], v[52:53], 0, v[40:41]
	v_and_b32_e32 v68, 0xfff800, v43
	v_lshl_add_u64 v[38:39], v[40:41], 0, v[68:69]
	global_load_dwordx2 v[166:167], v[38:39], off
	global_load_dwordx2 v[168:169], v[38:39], off offset:512
	global_load_dwordx2 v[170:171], v[38:39], off offset:1024
	global_load_dwordx2 v[172:173], v[38:39], off offset:1536
	s_waitcnt lgkmcnt(3)
	v_ashrrev_i32_e32 v45, 31, v44
	v_lshlrev_b64 v[44:45], 19, v[44:45]
	v_lshl_add_u64 v[44:45], v[52:53], 0, v[44:45]
	v_and_b32_e32 v68, 0xfff800, v54
	v_lshl_add_u64 v[38:39], v[44:45], 0, v[68:69]
	v_mul_f32_e32 v112, 0x3d800000, v47
	s_waitcnt lgkmcnt(2)
	v_ashrrev_i32_e32 v47, 31, v46
	global_load_dwordx2 v[174:175], v[38:39], off
	global_load_dwordx2 v[176:177], v[38:39], off offset:512
	global_load_dwordx2 v[178:179], v[38:39], off offset:1024
	global_load_dwordx2 v[180:181], v[38:39], off offset:1536
	v_lshlrev_b64 v[46:47], 19, v[46:47]
	v_lshl_add_u64 v[46:47], v[52:53], 0, v[46:47]
	v_and_b32_e32 v68, 0xfff800, v55
	v_lshl_add_u64 v[38:39], v[46:47], 0, v[68:69]
	v_mul_f32_e32 v78, 0x3d800000, v49
	s_waitcnt lgkmcnt(1)
	v_ashrrev_i32_e32 v49, 31, v48
	global_load_dwordx2 v[182:183], v[38:39], off
	global_load_dwordx2 v[184:185], v[38:39], off offset:512
	global_load_dwordx2 v[186:187], v[38:39], off offset:1024
	global_load_dwordx2 v[188:189], v[38:39], off offset:1536
	v_mul_f32_e32 v76, 0x3d800000, v51
	s_waitcnt lgkmcnt(0)
; template <int MODE>
; __device__ __forceinline__ void combine_phase(LAS unsigned char* ldsb, int bid, int G, const float* x, const float* gf, const bf16_t* Y, const u32x2* rec,
;                                               float* xout, const float* ng, const float* sc, const float* sh, bf16_t* hbuf) {
;     ...
;             for (int jj = 0; jj < 7; ++jj) { const int j = jb + jj; if (j > TOPK) break;
;                 size_t slot = (size_t)SLOT_SH + row; wj[jj] = Y8_INV;
;                 if (j < TOPK) { const int e = (int)(rr[j].x >> 13), pos = (int)(rr[j].x & 8191u); wj[jj] = __uint_as_float(rr[j].y) * Y8_INV; slot = (size_t)tstart[e] * BM + pos; }
;                 const unsigned char* yp = (const unsigned char*)Y + slot * D + lane * 8;
; #pragma unroll
;                 for (int i = 0; i < 4; ++i) yv[jj][i] = *(const u32x2*)(yp + i * 512);
;             }
; #pragma unroll
;             for (int jj = 0; jj < 7; ++jj) { const int j = jb + jj; if (j > TOPK) break; const float w = wj[jj];
; #pragma unroll
;                 for (int i = 0; i < 4; ++i) { const u32x2 y2 = yv[jj][i];
;                     const f32x2v p0 = __builtin_amdgcn_cvt_pk_f32_fp8((int)y2.x, false), p1 = __builtin_amdgcn_cvt_pk_f32_fp8((int)y2.x, true), p2 = __builtin_amdgcn_cvt_pk_f32_fp8((int)y2.y, false), p3 = __builtin_amdgcn_cvt_pk_f32_fp8((int)y2.y, true);
;                     a[i][0] += w * p0.x; a[i][1] += w * p0.y; a[i][2] += w * p1.x; a[i][3] += w * p1.y;
;                     a[i][4] += w * p2.x; a[i][5] += w * p2.y; a[i][6] += w * p3.x; a[i][7] += w * p3.y; }
;             }
	v_ashrrev_i32_e32 v51, 31, v50
	v_lshlrev_b64 v[48:49], 19, v[48:49]
	v_lshlrev_b64 v[50:51], 19, v[50:51]
	v_lshl_add_u64 v[48:49], v[52:53], 0, v[48:49]
	v_and_b32_e32 v68, 0xfff800, v56
	v_lshl_add_u64 v[50:51], v[52:53], 0, v[50:51]
	v_lshl_add_u64 v[38:39], v[48:49], 0, v[68:69]
	v_and_b32_e32 v68, 0xfff800, v57
	global_load_dwordx2 v[190:191], v[38:39], off
	global_load_dwordx2 v[192:193], v[38:39], off offset:512
	global_load_dwordx2 v[194:195], v[38:39], off offset:1024
	global_load_dwordx2 v[196:197], v[38:39], off offset:1536
	v_lshl_add_u64 v[38:39], v[50:51], 0, v[68:69]
	global_load_dwordx2 v[198:199], v[38:39], off
	global_load_dwordx2 v[200:201], v[38:39], off offset:512
	global_load_dwordx2 v[202:203], v[38:39], off offset:1024
	global_load_dwordx2 v[204:205], v[38:39], off offset:1536
	global_load_dwordx4 v[120:123], v34, s[8:9] offset:16
	global_load_dwordx4 v[124:127], v34, s[8:9]
	global_load_dwordx4 v[128:131], v132, s[8:9] offset:16
	s_nop 0
	global_load_dwordx4 v[132:135], v132, s[8:9]
	s_nop 0
	global_load_dwordx4 v[136:139], v36, s[8:9] offset:16
	global_load_dwordx4 v[140:143], v36, s[8:9]
	global_load_dwordx4 v[144:147], v42, s[8:9] offset:16
	global_load_dwordx4 v[148:151], v42, s[8:9]
	s_waitcnt vmcnt(39)
	v_cvt_pk_f32_fp8_e32 v[80:81], v60
	v_cvt_pk_f32_fp8_sdwa v[82:83], v60 src0_sel:WORD_1
	v_cvt_pk_f32_fp8_e32 v[84:85], v61
	v_cvt_pk_f32_fp8_sdwa v[86:87], v61 src0_sel:WORD_1
	s_waitcnt vmcnt(38)
	v_cvt_pk_f32_fp8_e32 v[88:89], v62
	v_cvt_pk_f32_fp8_sdwa v[90:91], v62 src0_sel:WORD_1
	v_cvt_pk_f32_fp8_e32 v[92:93], v63
	v_cvt_pk_f32_fp8_sdwa v[94:95], v63 src0_sel:WORD_1
	s_waitcnt vmcnt(37)
	v_cvt_pk_f32_fp8_e32 v[96:97], v64
	v_cvt_pk_f32_fp8_sdwa v[98:99], v64 src0_sel:WORD_1
	v_cvt_pk_f32_fp8_e32 v[100:101], v65
	v_cvt_pk_f32_fp8_sdwa v[102:103], v65 src0_sel:WORD_1
	global_load_dwordx4 v[54:57], v34, s[0:1] offset:16
	global_load_dwordx4 v[62:65], v34, s[0:1]
	global_load_dwordx4 v[46:49], v34, s[0:1] offset:2064
	global_load_dwordx4 v[58:61], v34, s[0:1] offset:2048
	global_load_dwordx4 v[38:41], v36, s[0:1] offset:16
	global_load_dwordx4 v[50:53], v36, s[0:1]
	s_nop 0
	global_load_dwordx4 v[34:37], v42, s[0:1] offset:16
	s_nop 0
	global_load_dwordx4 v[42:45], v42, s[0:1]
	s_waitcnt vmcnt(44)
	v_cvt_pk_f32_fp8_e32 v[104:105], v110
	v_cvt_pk_f32_fp8_sdwa v[106:107], v110 src0_sel:WORD_1
	v_cvt_pk_f32_fp8_e32 v[108:109], v111
	v_cvt_pk_f32_fp8_sdwa v[110:111], v111 src0_sel:WORD_1
	s_waitcnt vmcnt(39)
	v_cvt_pk_f32_fp8_e32 v[206:207], v158
	v_cvt_pk_f32_fp8_sdwa v[208:209], v158 src0_sel:WORD_1
	v_cvt_pk_f32_fp8_e32 v[210:211], v159
	v_cvt_pk_f32_fp8_sdwa v[158:159], v159 src0_sel:WORD_1
	s_waitcnt vmcnt(38)
	v_cvt_pk_f32_fp8_e32 v[212:213], v160
	v_cvt_pk_f32_fp8_sdwa v[214:215], v160 src0_sel:WORD_1
	v_cvt_pk_f32_fp8_e32 v[216:217], v161
	v_cvt_pk_f32_fp8_sdwa v[160:161], v161 src0_sel:WORD_1
	s_waitcnt vmcnt(37)
	v_cvt_pk_f32_fp8_e32 v[218:219], v162
	v_cvt_pk_f32_fp8_sdwa v[220:221], v162 src0_sel:WORD_1
	v_cvt_pk_f32_fp8_e32 v[222:223], v163
	v_cvt_pk_f32_fp8_sdwa v[162:163], v163 src0_sel:WORD_1
	s_waitcnt vmcnt(36)
	v_cvt_pk_f32_fp8_e32 v[224:225], v164
	v_cvt_pk_f32_fp8_sdwa v[226:227], v164 src0_sel:WORD_1
	v_cvt_pk_f32_fp8_e32 v[228:229], v165
	v_cvt_pk_f32_fp8_sdwa v[164:165], v165 src0_sel:WORD_1
	s_waitcnt vmcnt(35)
	v_cvt_pk_f32_fp8_e32 v[230:231], v166
	v_cvt_pk_f32_fp8_sdwa v[232:233], v166 src0_sel:WORD_1
	s_waitcnt vmcnt(34)
	v_cvt_pk_f32_fp8_e32 v[236:237], v168
	v_pk_fma_f32 v[206:207], v[152:153], v[206:207], 0 op_sel_hi:[0,1,0]
	v_cvt_pk_f32_fp8_e32 v[234:235], v167
	v_cvt_pk_f32_fp8_sdwa v[166:167], v167 src0_sel:WORD_1
	v_cvt_pk_f32_fp8_sdwa v[238:239], v168 src0_sel:WORD_1
	v_cvt_pk_f32_fp8_e32 v[240:241], v169
	v_cvt_pk_f32_fp8_sdwa v[168:169], v169 src0_sel:WORD_1
	v_pk_fma_f32 v[208:209], v[152:153], v[208:209], 0 op_sel_hi:[0,1,0]
	v_pk_fma_f32 v[210:211], v[152:153], v[210:211], 0 op_sel_hi:[0,1,0]
	v_pk_fma_f32 v[158:159], v[152:153], v[158:159], 0 op_sel_hi:[0,1,0]
	v_pk_fma_f32 v[212:213], v[152:153], v[212:213], 0 op_sel_hi:[0,1,0]
	v_pk_fma_f32 v[214:215], v[152:153], v[214:215], 0 op_sel_hi:[0,1,0]
	v_pk_fma_f32 v[216:217], v[152:153], v[216:217], 0 op_sel_hi:[0,1,0]
	v_pk_fma_f32 v[160:161], v[152:153], v[160:161], 0 op_sel_hi:[0,1,0]
	v_pk_fma_f32 v[218:219], v[152:153], v[218:219], 0 op_sel_hi:[0,1,0]
	v_pk_fma_f32 v[220:221], v[152:153], v[220:221], 0 op_sel_hi:[0,1,0]
	v_pk_fma_f32 v[222:223], v[152:153], v[222:223], 0 op_sel_hi:[0,1,0]
	v_pk_fma_f32 v[162:163], v[152:153], v[162:163], 0 op_sel_hi:[0,1,0]
	v_pk_fma_f32 v[224:225], v[152:153], v[224:225], 0 op_sel_hi:[0,1,0]
	v_pk_fma_f32 v[226:227], v[152:153], v[226:227], 0 op_sel_hi:[0,1,0]
	v_pk_fma_f32 v[228:229], v[152:153], v[228:229], 0 op_sel_hi:[0,1,0]
	v_pk_fma_f32 v[152:153], v[152:153], v[164:165], 0 op_sel_hi:[0,1,0]
	s_waitcnt vmcnt(33)
	v_cvt_pk_f32_fp8_e32 v[164:165], v170
	v_pk_fma_f32 v[206:207], v[154:155], v[230:231], v[206:207] op_sel_hi:[0,1,1]
	v_cvt_pk_f32_fp8_sdwa v[230:231], v170 src0_sel:WORD_1
	v_pk_fma_f32 v[208:209], v[154:155], v[232:233], v[208:209] op_sel_hi:[0,1,1]
	v_cvt_pk_f32_fp8_e32 v[232:233], v171
	v_pk_fma_f32 v[212:213], v[154:155], v[236:237], v[212:213] op_sel_hi:[0,1,1]
	s_waitcnt vmcnt(32)
	v_cvt_pk_f32_fp8_e32 v[236:237], v173
	v_cvt_pk_f32_fp8_sdwa v[170:171], v171 src0_sel:WORD_1
	v_pk_fma_f32 v[210:211], v[154:155], v[234:235], v[210:211] op_sel_hi:[0,1,1]
	v_cvt_pk_f32_fp8_e32 v[234:235], v172
	v_pk_fma_f32 v[158:159], v[154:155], v[166:167], v[158:159] op_sel_hi:[0,1,1]
	v_cvt_pk_f32_fp8_sdwa v[166:167], v172 src0_sel:WORD_1
	v_cvt_pk_f32_fp8_sdwa v[172:173], v173 src0_sel:WORD_1
	v_pk_fma_f32 v[214:215], v[154:155], v[238:239], v[214:215] op_sel_hi:[0,1,1]
	s_waitcnt vmcnt(31)
; template <int MODE>
; __device__ __forceinline__ void combine_phase(LAS unsigned char* ldsb, int bid, int G, const float* x, const float* gf, const bf16_t* Y, const u32x2* rec,
;                                               float* xout, const float* ng, const float* sc, const float* sh, bf16_t* hbuf) {
;     ...
;             for (int jj = 0; jj < 7; ++jj) { const int j = jb + jj; if (j > TOPK) break; const float w = wj[jj];
; #pragma unroll
;                 for (int i = 0; i < 4; ++i) { const u32x2 y2 = yv[jj][i];
;                     const f32x2v p0 = __builtin_amdgcn_cvt_pk_f32_fp8((int)y2.x, false), p1 = __builtin_amdgcn_cvt_pk_f32_fp8((int)y2.x, true), p2 = __builtin_amdgcn_cvt_pk_f32_fp8((int)y2.y, false), p3 = __builtin_amdgcn_cvt_pk_f32_fp8((int)y2.y, true);
;                     a[i][0] += w * p0.x; a[i][1] += w * p0.y; a[i][2] += w * p1.x; a[i][3] += w * p1.y;
;                     a[i][4] += w * p2.x; a[i][5] += w * p2.y; a[i][6] += w * p3.x; a[i][7] += w * p3.y; }
;             }
	v_cvt_pk_f32_fp8_e32 v[238:239], v174
	v_pk_fma_f32 v[216:217], v[154:155], v[240:241], v[216:217] op_sel_hi:[0,1,1]
	v_cvt_pk_f32_fp8_sdwa v[240:241], v174 src0_sel:WORD_1
	v_pk_fma_f32 v[160:161], v[154:155], v[168:169], v[160:161] op_sel_hi:[0,1,1]
	v_cvt_pk_f32_fp8_e32 v[168:169], v175
	v_cvt_pk_f32_fp8_sdwa v[174:175], v175 src0_sel:WORD_1
	v_pk_fma_f32 v[164:165], v[154:155], v[164:165], v[218:219] op_sel_hi:[0,1,1]
	s_waitcnt vmcnt(30)
	v_cvt_pk_f32_fp8_e32 v[218:219], v176
	v_pk_fma_f32 v[220:221], v[154:155], v[230:231], v[220:221] op_sel_hi:[0,1,1]
	v_cvt_pk_f32_fp8_sdwa v[230:231], v176 src0_sel:WORD_1
	v_pk_fma_f32 v[222:223], v[154:155], v[232:233], v[222:223] op_sel_hi:[0,1,1]
	v_cvt_pk_f32_fp8_e32 v[232:233], v177
	v_cvt_pk_f32_fp8_sdwa v[176:177], v177 src0_sel:WORD_1
	v_pk_fma_f32 v[228:229], v[154:155], v[236:237], v[228:229] op_sel_hi:[0,1,1]
	s_waitcnt vmcnt(28)
	v_cvt_pk_f32_fp8_e32 v[236:237], v180
	v_pk_fma_f32 v[162:163], v[154:155], v[170:171], v[162:163] op_sel_hi:[0,1,1]
	v_cvt_pk_f32_fp8_e32 v[170:171], v178
	v_pk_fma_f32 v[224:225], v[154:155], v[234:235], v[224:225] op_sel_hi:[0,1,1]
	v_pk_fma_f32 v[166:167], v[154:155], v[166:167], v[226:227] op_sel_hi:[0,1,1]
	v_pk_fma_f32 v[152:153], v[154:155], v[172:173], v[152:153] op_sel_hi:[0,1,1]
	v_cvt_pk_f32_fp8_sdwa v[154:155], v180 src0_sel:WORD_1
	v_pk_fma_f32 v[158:159], v[156:157], v[174:175], v[158:159] op_sel_hi:[0,1,1]
	s_waitcnt vmcnt(26)
	v_cvt_pk_f32_fp8_e32 v[174:175], v184
	v_pk_fma_f32 v[212:213], v[156:157], v[218:219], v[212:213] op_sel_hi:[0,1,1]
	v_cvt_pk_f32_fp8_sdwa v[218:219], v184 src0_sel:WORD_1
	v_pk_fma_f32 v[214:215], v[156:157], v[230:231], v[214:215] op_sel_hi:[0,1,1]
	v_cvt_pk_f32_fp8_e32 v[230:231], v185
	v_cvt_pk_f32_fp8_sdwa v[184:185], v185 src0_sel:WORD_1
	v_pk_fma_f32 v[216:217], v[156:157], v[232:233], v[216:217] op_sel_hi:[0,1,1]
	s_waitcnt vmcnt(25)
	v_cvt_pk_f32_fp8_e32 v[232:233], v186
	v_cvt_pk_f32_fp8_sdwa v[234:235], v178 src0_sel:WORD_1
	v_cvt_pk_f32_fp8_e32 v[172:173], v181
	v_pk_fma_f32 v[206:207], v[156:157], v[238:239], v[206:207] op_sel_hi:[0,1,1]
	v_cvt_pk_f32_fp8_e32 v[238:239], v182
	v_pk_fma_f32 v[208:209], v[156:157], v[240:241], v[208:209] op_sel_hi:[0,1,1]
	v_cvt_pk_f32_fp8_sdwa v[240:241], v182 src0_sel:WORD_1
	v_pk_fma_f32 v[160:161], v[156:157], v[176:177], v[160:161] op_sel_hi:[0,1,1]
	v_cvt_pk_f32_fp8_sdwa v[176:177], v186 src0_sel:WORD_1
	v_pk_fma_f32 v[224:225], v[156:157], v[236:237], v[224:225] op_sel_hi:[0,1,1]
	s_waitcnt vmcnt(23)
	v_cvt_pk_f32_fp8_e32 v[236:237], v190
	v_pk_fma_f32 v[164:165], v[156:157], v[170:171], v[164:165] op_sel_hi:[0,1,1]
	v_pk_fma_f32 v[154:155], v[156:157], v[154:155], v[166:167] op_sel_hi:[0,1,1]
	v_cvt_pk_f32_fp8_sdwa v[166:167], v190 src0_sel:WORD_1
	v_pk_fma_f32 v[160:161], v[112:113], v[184:185], v[160:161] op_sel_hi:[0,1,1]
	s_waitcnt vmcnt(19)
	v_cvt_pk_f32_fp8_e32 v[184:185], v198
	v_pk_fma_f32 v[168:169], v[156:157], v[168:169], v[210:211] op_sel_hi:[0,1,1]
	v_cvt_pk_f32_fp8_e32 v[210:211], v183
	v_pk_fma_f32 v[164:165], v[112:113], v[232:233], v[164:165] op_sel_hi:[0,1,1]
	v_cvt_pk_f32_fp8_sdwa v[232:233], v198 src0_sel:WORD_1
	v_cvt_pk_f32_fp8_e32 v[226:227], v179
	v_cvt_pk_f32_fp8_sdwa v[178:179], v179 src0_sel:WORD_1
	v_cvt_pk_f32_fp8_sdwa v[180:181], v181 src0_sel:WORD_1
	v_pk_fma_f32 v[220:221], v[156:157], v[234:235], v[220:221] op_sel_hi:[0,1,1]
	v_pk_fma_f32 v[172:173], v[156:157], v[172:173], v[228:229] op_sel_hi:[0,1,1]
	v_cvt_pk_f32_fp8_e32 v[228:229], v191
	v_pk_fma_f32 v[206:207], v[112:113], v[238:239], v[206:207] op_sel_hi:[0,1,1]
	v_cvt_pk_f32_fp8_sdwa v[182:183], v183 src0_sel:WORD_1
	v_cvt_pk_f32_fp8_e32 v[170:171], v187
	v_pk_fma_f32 v[208:209], v[112:113], v[240:241], v[208:209] op_sel_hi:[0,1,1]
	v_pk_fma_f32 v[176:177], v[112:113], v[176:177], v[220:221] op_sel_hi:[0,1,1]
	v_cvt_pk_f32_fp8_e32 v[220:221], v199
	v_pk_fma_f32 v[206:207], v[78:79], v[236:237], v[206:207] op_sel_hi:[0,1,1]
	v_cvt_pk_f32_fp8_sdwa v[190:191], v191 src0_sel:WORD_1
	v_pk_fma_f32 v[166:167], v[78:79], v[166:167], v[208:209] op_sel_hi:[0,1,1]
	v_pk_fma_f32 v[184:185], v[76:77], v[184:185], v[206:207] op_sel_hi:[0,1,1]
	v_cvt_pk_f32_fp8_sdwa v[186:187], v187 src0_sel:WORD_1
	v_pk_fma_f32 v[168:169], v[112:113], v[210:211], v[168:169] op_sel_hi:[0,1,1]
	v_cvt_pk_f32_fp8_sdwa v[198:199], v199 src0_sel:WORD_1
	v_pk_fma_f32 v[166:167], v[76:77], v[232:233], v[166:167] op_sel_hi:[0,1,1]
	v_pk_fma_f32 v[80:81], v[80:81], s[6:7], v[184:185] op_sel_hi:[1,0,1]
	v_pk_fma_f32 v[222:223], v[156:157], v[226:227], v[222:223] op_sel_hi:[0,1,1]
	v_pk_fma_f32 v[162:163], v[156:157], v[178:179], v[162:163] op_sel_hi:[0,1,1]
	v_pk_fma_f32 v[152:153], v[156:157], v[180:181], v[152:153] op_sel_hi:[0,1,1]
	v_cvt_pk_f32_fp8_e32 v[156:157], v192
	v_pk_fma_f32 v[168:169], v[78:79], v[228:229], v[168:169] op_sel_hi:[0,1,1]
	v_pk_fma_f32 v[82:83], v[82:83], s[6:7], v[166:167] op_sel_hi:[1,0,1]
	s_waitcnt vmcnt(14)
; template <int MODE>
; __device__ __forceinline__ void combine_phase(LAS unsigned char* ldsb, int bid, int G, const float* x, const float* gf, const bf16_t* Y, const u32x2* rec,
;                                               float* xout, const float* ng, const float* sc, const float* sh, bf16_t* hbuf) {
;     ...
;         float ss = 0.f;
; #pragma unroll
;         for (int i = 0; i < 4; ++i) { const int c = lane * 8 + i * 512;
; #pragma unroll
;             for (int h = 0; h < 2; ++h) { const float4 xv = xr[i][h], gv = *(const float4*)(gf + c + h * 4);
;                 a[i][h * 4 + 0] = xv.x + gv.x * a[i][h * 4 + 0]; a[i][h * 4 + 1] = xv.y + gv.y * a[i][h * 4 + 1]; a[i][h * 4 + 2] = xv.z + gv.z * a[i][h * 4 + 2]; a[i][h * 4 + 3] = xv.w + gv.w * a[i][h * 4 + 3]; }
; #pragma unroll
;             for (int q = 0; q < 8; ++q) ss += a[i][q] * a[i][q]; }
	v_pk_fma_f32 v[18:19], v[80:81], v[124:125], v[18:19]
	v_cvt_pk_f32_fp8_e32 v[234:235], v188
	v_pk_fma_f32 v[158:159], v[112:113], v[182:183], v[158:159] op_sel_hi:[0,1,1]
	v_pk_fma_f32 v[170:171], v[112:113], v[170:171], v[222:223] op_sel_hi:[0,1,1]
	v_cvt_pk_f32_fp8_e32 v[222:223], v200
	v_pk_fma_f32 v[168:169], v[76:77], v[220:221], v[168:169] op_sel_hi:[0,1,1]
	v_pk_fma_f32 v[20:21], v[82:83], v[126:127], v[20:21]
	v_pk_mul_f32 v[80:81], v[18:19], v[18:19]
	v_cvt_pk_f32_fp8_sdwa v[180:181], v192 src0_sel:WORD_1
	v_pk_fma_f32 v[158:159], v[78:79], v[190:191], v[158:159] op_sel_hi:[0,1,1]
	v_pk_fma_f32 v[84:85], v[84:85], s[6:7], v[168:169] op_sel_hi:[1,0,1]
	v_pk_mul_f32 v[82:83], v[20:21], v[20:21]
	v_add_f32_e32 v68, v80, v81
	v_pk_fma_f32 v[174:175], v[112:113], v[174:175], v[212:213] op_sel_hi:[0,1,1]
	v_pk_fma_f32 v[162:163], v[112:113], v[186:187], v[162:163] op_sel_hi:[0,1,1]
	v_cvt_pk_f32_fp8_sdwa v[186:187], v200 src0_sel:WORD_1
	v_pk_fma_f32 v[158:159], v[76:77], v[198:199], v[158:159] op_sel_hi:[0,1,1]
	v_pk_fma_f32 v[6:7], v[84:85], v[120:121], v[6:7]
	v_add_f32_e32 v68, v68, v82
	v_cvt_pk_f32_fp8_e32 v[238:239], v193
	v_pk_fma_f32 v[156:157], v[78:79], v[156:157], v[174:175] op_sel_hi:[0,1,1]
	v_pk_fma_f32 v[86:87], v[86:87], s[6:7], v[158:159] op_sel_hi:[1,0,1]
	v_pk_mul_f32 v[84:85], v[6:7], v[6:7]
	v_add_f32_e32 v68, v68, v83
	v_cvt_pk_f32_fp8_sdwa v[226:227], v188 src0_sel:WORD_1
	v_pk_fma_f32 v[214:215], v[112:113], v[218:219], v[214:215] op_sel_hi:[0,1,1]
	v_pk_fma_f32 v[224:225], v[112:113], v[234:235], v[224:225] op_sel_hi:[0,1,1]
	v_cvt_pk_f32_fp8_e32 v[234:235], v201
	v_pk_fma_f32 v[156:157], v[76:77], v[222:223], v[156:157] op_sel_hi:[0,1,1]
	v_pk_fma_f32 v[8:9], v[86:87], v[122:123], v[8:9]
	v_add_f32_e32 v68, v68, v84
	v_cvt_pk_f32_fp8_sdwa v[192:193], v193 src0_sel:WORD_1
	v_pk_fma_f32 v[174:175], v[78:79], v[180:181], v[214:215] op_sel_hi:[0,1,1]
	v_pk_fma_f32 v[88:89], v[88:89], s[6:7], v[156:157] op_sel_hi:[1,0,1]
	v_pk_mul_f32 v[86:87], v[8:9], v[8:9]
	v_add_f32_e32 v68, v68, v85
	v_cvt_pk_f32_fp8_e32 v[178:179], v189
	v_pk_fma_f32 v[216:217], v[112:113], v[230:231], v[216:217] op_sel_hi:[0,1,1]
	v_cvt_pk_f32_fp8_sdwa v[200:201], v201 src0_sel:WORD_1
	v_pk_fma_f32 v[174:175], v[76:77], v[186:187], v[174:175] op_sel_hi:[0,1,1]
	s_waitcnt vmcnt(12)
	v_pk_fma_f32 v[10:11], v[88:89], v[132:133], v[10:11]
	v_add_f32_e32 v68, v68, v86
	v_cvt_pk_f32_fp8_e32 v[240:241], v194
	v_pk_fma_f32 v[180:181], v[78:79], v[238:239], v[216:217] op_sel_hi:[0,1,1]
	v_pk_fma_f32 v[90:91], v[90:91], s[6:7], v[174:175] op_sel_hi:[1,0,1]
	v_pk_mul_f32 v[88:89], v[10:11], v[10:11]
	v_add_f32_e32 v68, v68, v87
	v_cvt_pk_f32_fp8_sdwa v[188:189], v189 src0_sel:WORD_1
	v_pk_fma_f32 v[154:155], v[112:113], v[226:227], v[154:155] op_sel_hi:[0,1,1]
	v_cvt_pk_f32_fp8_e32 v[226:227], v202
	v_pk_fma_f32 v[180:181], v[76:77], v[234:235], v[180:181] op_sel_hi:[0,1,1]
	v_pk_fma_f32 v[12:13], v[90:91], v[134:135], v[12:13]
	v_add_f32_e32 v68, v68, v88
	v_cvt_pk_f32_fp8_sdwa v[210:211], v194 src0_sel:WORD_1
	v_pk_fma_f32 v[160:161], v[78:79], v[192:193], v[160:161] op_sel_hi:[0,1,1]
	v_pk_fma_f32 v[92:93], v[92:93], s[6:7], v[180:181] op_sel_hi:[1,0,1]
	v_pk_mul_f32 v[90:91], v[12:13], v[12:13]
	v_add_f32_e32 v68, v68, v89
	v_pk_fma_f32 v[172:173], v[112:113], v[178:179], v[172:173] op_sel_hi:[0,1,1]
	v_cvt_pk_f32_fp8_sdwa v[178:179], v202 src0_sel:WORD_1
	v_pk_fma_f32 v[160:161], v[76:77], v[200:201], v[160:161] op_sel_hi:[0,1,1]
	v_pk_fma_f32 v[2:3], v[92:93], v[128:129], v[2:3]
	v_add_f32_e32 v68, v68, v90
	v_cvt_pk_f32_fp8_e32 v[182:183], v195
	v_pk_fma_f32 v[164:165], v[78:79], v[240:241], v[164:165] op_sel_hi:[0,1,1]
	v_pk_fma_f32 v[94:95], v[94:95], s[6:7], v[160:161] op_sel_hi:[1,0,1]
	v_pk_mul_f32 v[92:93], v[2:3], v[2:3]
	v_add_f32_e32 v68, v68, v91
	v_pk_fma_f32 v[152:153], v[112:113], v[188:189], v[152:153] op_sel_hi:[0,1,1]
	v_cvt_pk_f32_fp8_e32 v[188:189], v203
	v_pk_fma_f32 v[164:165], v[76:77], v[226:227], v[164:165] op_sel_hi:[0,1,1]
	v_pk_fma_f32 v[4:5], v[94:95], v[130:131], v[4:5]
	v_add_f32_e32 v68, v68, v92
	v_cvt_pk_f32_fp8_sdwa v[194:195], v195 src0_sel:WORD_1
	v_pk_fma_f32 v[176:177], v[78:79], v[210:211], v[176:177] op_sel_hi:[0,1,1]
	v_pk_fma_f32 v[96:97], v[96:97], s[6:7], v[164:165] op_sel_hi:[1,0,1]
	v_pk_mul_f32 v[94:95], v[4:5], v[4:5]
	v_add_f32_e32 v68, v68, v93
	v_cvt_pk_f32_fp8_sdwa v[202:203], v203 src0_sel:WORD_1
	v_pk_fma_f32 v[176:177], v[76:77], v[178:179], v[176:177] op_sel_hi:[0,1,1]
	s_waitcnt vmcnt(10)
; __device__ __forceinline__ unsigned cvt_pk_bf16(float lo, float hi) { unsigned r; asm volatile("v_cvt_pk_bf16_f32 %0, %1, %2" : "=v"(r) : "v"(lo), "v"(hi)); return r; }
; template <int MODE>
; __device__ __forceinline__ void combine_phase(LAS unsigned char* ldsb, int bid, int G, const float* x, const float* gf, const bf16_t* Y, const u32x2* rec,
;                                               float* xout, const float* ng, const float* sc, const float* sh, bf16_t* hbuf) {
;     ...
;         if (MODE == 0 || MODE == 2) {
; #pragma unroll
;             for (int i = 0; i < 4; ++i) { float* op = xout + (size_t)row * D + lane * 8 + i * 512; *(float4*)op = make_float4(a[i][0], a[i][1], a[i][2], a[i][3]); *(float4*)(op + 4) = make_float4(a[i][4], a[i][5], a[i][6], a[i][7]); }
;         }
;         if (MODE == 1 || MODE == 2) {
;             ss = wave_sum(ss);
;             const float r = rsqrtf(ss * (1.f / D) + EPS);
;             asm volatile("" ::: "memory");
;             float4 g4[4][2];
; #pragma unroll
;             for (int i = 0; i < 4; ++i) { const int c = lane * 8 + i * 512; g4[i][0] = *(const float4*)(ng + c); g4[i][1] = *(const float4*)(ng + c + 4); }
; #pragma unroll
;             for (int i = 0; i < 4; ++i) { const int c = lane * 8 + i * 512; float o[8];
;                 const float gq[8] = {g4[i][0].x, g4[i][0].y, g4[i][0].z, g4[i][0].w, g4[i][1].x, g4[i][1].y, g4[i][1].z, g4[i][1].w};
; #pragma unroll
;                 for (int q = 0; q < 8; ++q) { o[q] = a[i][q] * r * gq[q]; if (MODE == 2) o[q] = o[q] * (1.f + sc[c + q]) + sh[c + q]; }
;                 if (MODE == 1) { float* op = xout + (size_t)row * D + c; *(float4*)op = make_float4(o[0], o[1], o[2], o[3]); *(float4*)(op + 4) = make_float4(o[4], o[5], o[6], o[7]); }
;                 else { u32x4 w; w.x = cvt_pk_bf16(o[0], o[1]); w.y = cvt_pk_bf16(o[2], o[3]); w.z = cvt_pk_bf16(o[4], o[5]); w.w = cvt_pk_bf16(o[6], o[7]); *(u32x4*)(hbuf + (size_t)row * D + c) = w; } }
	v_pk_fma_f32 v[30:31], v[96:97], v[140:141], v[30:31]
	v_add_f32_e32 v68, v68, v94
	v_cvt_pk_f32_fp8_e32 v[212:213], v196
	v_pk_fma_f32 v[170:171], v[78:79], v[182:183], v[170:171] op_sel_hi:[0,1,1]
	v_pk_fma_f32 v[98:99], v[98:99], s[6:7], v[176:177] op_sel_hi:[1,0,1]
	v_pk_mul_f32 v[96:97], v[30:31], v[30:31]
	v_add_f32_e32 v68, v68, v95
	v_cvt_pk_f32_fp8_e32 v[242:243], v204
	v_pk_fma_f32 v[170:171], v[76:77], v[188:189], v[170:171] op_sel_hi:[0,1,1]
	v_pk_fma_f32 v[32:33], v[98:99], v[142:143], v[32:33]
	v_add_f32_e32 v68, v68, v96
	v_cvt_pk_f32_fp8_sdwa v[218:219], v196 src0_sel:WORD_1
	v_pk_fma_f32 v[162:163], v[78:79], v[194:195], v[162:163] op_sel_hi:[0,1,1]
	v_pk_fma_f32 v[100:101], v[100:101], s[6:7], v[170:171] op_sel_hi:[1,0,1]
	v_pk_mul_f32 v[98:99], v[32:33], v[32:33]
	v_add_f32_e32 v68, v68, v97
	v_cvt_pk_f32_fp8_sdwa v[236:237], v204 src0_sel:WORD_1
	v_pk_fma_f32 v[162:163], v[76:77], v[202:203], v[162:163] op_sel_hi:[0,1,1]
	v_pk_fma_f32 v[22:23], v[100:101], v[136:137], v[22:23]
	v_add_f32_e32 v68, v68, v98
	v_cvt_pk_f32_fp8_e32 v[230:231], v197
	v_pk_fma_f32 v[182:183], v[78:79], v[212:213], v[224:225] op_sel_hi:[0,1,1]
	v_pk_fma_f32 v[102:103], v[102:103], s[6:7], v[162:163] op_sel_hi:[1,0,1]
	v_pk_mul_f32 v[100:101], v[22:23], v[22:23]
	v_add_f32_e32 v68, v68, v99
	v_cvt_pk_f32_fp8_e32 v[208:209], v205
	v_pk_fma_f32 v[178:179], v[76:77], v[242:243], v[182:183] op_sel_hi:[0,1,1]
	v_pk_fma_f32 v[24:25], v[102:103], v[138:139], v[24:25]
	v_add_f32_e32 v68, v68, v100
	v_cvt_pk_f32_fp8_sdwa v[196:197], v197 src0_sel:WORD_1
	v_pk_fma_f32 v[154:155], v[78:79], v[218:219], v[154:155] op_sel_hi:[0,1,1]
	v_pk_fma_f32 v[104:105], v[104:105], s[6:7], v[178:179] op_sel_hi:[1,0,1]
	v_pk_mul_f32 v[102:103], v[24:25], v[24:25]
	v_add_f32_e32 v68, v68, v101
	v_cvt_pk_f32_fp8_sdwa v[204:205], v205 src0_sel:WORD_1
	v_pk_fma_f32 v[154:155], v[76:77], v[236:237], v[154:155] op_sel_hi:[0,1,1]
	s_waitcnt vmcnt(8)
	v_pk_fma_f32 v[26:27], v[104:105], v[148:149], v[26:27]
	v_add_f32_e32 v68, v68, v102
	v_pk_fma_f32 v[172:173], v[78:79], v[230:231], v[172:173] op_sel_hi:[0,1,1]
	v_pk_fma_f32 v[106:107], v[106:107], s[6:7], v[154:155] op_sel_hi:[1,0,1]
	v_pk_mul_f32 v[104:105], v[26:27], v[26:27]
	v_add_f32_e32 v68, v68, v103
	v_pk_fma_f32 v[172:173], v[76:77], v[208:209], v[172:173] op_sel_hi:[0,1,1]
	v_pk_fma_f32 v[28:29], v[106:107], v[150:151], v[28:29]
	v_add_f32_e32 v68, v68, v104
	v_pk_fma_f32 v[152:153], v[78:79], v[196:197], v[152:153] op_sel_hi:[0,1,1]
	v_pk_fma_f32 v[108:109], v[108:109], s[6:7], v[172:173] op_sel_hi:[1,0,1]
	v_pk_mul_f32 v[106:107], v[28:29], v[28:29]
	v_add_f32_e32 v68, v68, v105
	v_pk_fma_f32 v[152:153], v[76:77], v[204:205], v[152:153] op_sel_hi:[0,1,1]
	v_pk_fma_f32 v[14:15], v[108:109], v[144:145], v[14:15]
	v_add_f32_e32 v68, v68, v106
	v_pk_fma_f32 v[110:111], v[110:111], s[6:7], v[152:153] op_sel_hi:[1,0,1]
	v_pk_mul_f32 v[108:109], v[14:15], v[14:15]
	v_add_f32_e32 v68, v68, v107
	v_pk_fma_f32 v[16:17], v[110:111], v[146:147], v[16:17]
	v_add_f32_e32 v68, v68, v108
	v_pk_mul_f32 v[110:111], v[16:17], v[16:17]
	v_add_f32_e32 v68, v68, v109
	v_add_f32_e32 v68, v68, v110
	v_add_f32_e32 v68, v68, v111
	ds_bpermute_b32 v67, v67, v68
	s_waitcnt lgkmcnt(0)
	v_add_f32_e32 v67, v68, v67
	ds_bpermute_b32 v68, v244, v67
	s_waitcnt lgkmcnt(0)
	v_add_f32_e32 v67, v67, v68
	ds_bpermute_b32 v68, v245, v67
	s_waitcnt lgkmcnt(0)
	v_add_f32_e32 v67, v67, v68
	ds_bpermute_b32 v68, v246, v67
	s_waitcnt lgkmcnt(0)
	v_add_f32_e32 v67, v67, v68
	ds_bpermute_b32 v68, v247, v67
	s_waitcnt lgkmcnt(0)
	v_add_f32_e32 v67, v67, v68
	ds_bpermute_b32 v68, v248, v67
	s_waitcnt lgkmcnt(0)
	v_add_f32_e32 v67, v67, v68
	v_fmamk_f32 v67, v67, 0x3a000000, v118
	v_mul_f32_e32 v68, 0x4b800000, v67
	v_cmp_gt_f32_e32 vcc, s15, v67
	s_nop 1
	v_cndmask_b32_e32 v67, v67, v68, vcc
	v_rsq_f32_e32 v67, v67
	s_nop 0
	v_mul_f32_e32 v68, 0x45800000, v67
	v_cndmask_b32_e32 v68, v67, v68, vcc
	v_pk_mul_f32 v[18:19], v[18:19], v[68:69] op_sel_hi:[1,0]
	v_pk_mul_f32 v[20:21], v[20:21], v[68:69] op_sel_hi:[1,0]
	v_pk_mul_f32 v[6:7], v[6:7], v[68:69] op_sel_hi:[1,0]
	v_pk_mul_f32 v[8:9], v[8:9], v[68:69] op_sel_hi:[1,0]
	v_pk_mul_f32 v[10:11], v[10:11], v[68:69] op_sel_hi:[1,0]
	v_pk_mul_f32 v[12:13], v[12:13], v[68:69] op_sel_hi:[1,0]
	v_pk_mul_f32 v[80:81], v[2:3], v[68:69] op_sel_hi:[1,0]
	v_pk_mul_f32 v[82:83], v[4:5], v[68:69] op_sel_hi:[1,0]
	v_pk_mul_f32 v[30:31], v[30:31], v[68:69] op_sel_hi:[1,0]
	v_pk_mul_f32 v[32:33], v[32:33], v[68:69] op_sel_hi:[1,0]
	v_pk_mul_f32 v[22:23], v[22:23], v[68:69] op_sel_hi:[1,0]
	v_pk_mul_f32 v[24:25], v[24:25], v[68:69] op_sel_hi:[1,0]
	v_pk_mul_f32 v[26:27], v[26:27], v[68:69] op_sel_hi:[1,0]
	v_pk_mul_f32 v[28:29], v[28:29], v[68:69] op_sel_hi:[1,0]
	v_pk_mul_f32 v[84:85], v[14:15], v[68:69] op_sel_hi:[1,0]
	v_pk_mul_f32 v[86:87], v[16:17], v[68:69] op_sel_hi:[1,0]
	s_waitcnt vmcnt(6)
	v_pk_mul_f32 v[2:3], v[62:63], v[18:19]
	v_pk_mul_f32 v[4:5], v[64:65], v[20:21]
	v_pk_mul_f32 v[6:7], v[54:55], v[6:7]
	v_pk_mul_f32 v[8:9], v[56:57], v[8:9]
	s_waitcnt vmcnt(4)
	v_pk_mul_f32 v[10:11], v[58:59], v[10:11]
	v_pk_mul_f32 v[12:13], v[12:13], v[60:61]
	v_pk_mul_f32 v[14:15], v[80:81], v[46:47]
	v_pk_mul_f32 v[16:17], v[82:83], v[48:49]
	s_waitcnt vmcnt(2)
	v_pk_mul_f32 v[18:19], v[30:31], v[50:51]
	v_pk_mul_f32 v[20:21], v[32:33], v[52:53]
	v_pk_mul_f32 v[22:23], v[22:23], v[38:39]
	v_pk_mul_f32 v[24:25], v[24:25], v[40:41]
	s_waitcnt vmcnt(0)
	v_pk_mul_f32 v[26:27], v[26:27], v[42:43]
	v_pk_mul_f32 v[28:29], v[28:29], v[44:45]
	v_pk_mul_f32 v[30:31], v[84:85], v[34:35]
	v_pk_mul_f32 v[32:33], v[86:87], v[36:37]
	global_store_dwordx4 v[70:71], v[2:5], off nt
	global_store_dwordx4 v[70:71], v[6:9], off offset:16 nt
	global_store_dwordx4 v[70:71], v[10:13], off offset:2048 nt
	global_store_dwordx4 v[70:71], v[14:17], off offset:2064 nt
	global_store_dwordx4 v[74:75], v[18:21], off nt
	global_store_dwordx4 v[74:75], v[22:25], off offset:16 nt
	global_store_dwordx4 v[72:73], v[26:29], off nt
	global_store_dwordx4 v[72:73], v[30:33], off offset:16 nt
	s_andn2_b64 exec, exec, s[4:5]
	s_cbranch_execnz .LBB0_1958
